# P7 token loop: LN/modulation rows from LDS+registers, g1 loads hoisted before the next-token prefetch, counted vmcnt so the prefetch overlaps the token
# speedup vs baseline: 1.0350x; 1.0014x over previous
.LBB0_838:
	s_ashr_i32 s4, s48, 31
	s_lshr_b32 s4, s4, 26
	s_lshl_b32 s49, s48, 5
	s_add_i32 s4, s48, s4
	s_lshr_b32 s4, s4, 6
	s_add_i32 s6, s49, s25
	s_mulk_i32 s4, 0x3000
	s_ashr_i32 s7, s6, 31
	s_ashr_i32 s5, s4, 31
	s_lshl_b64 s[8:9], s[6:7], 13
	s_add_u32 s8, s28, s8
	s_addc_u32 s9, s29, s9
	s_lshl_b64 s[10:11], s[6:7], 12
	v_lshl_add_u64 v[26:27], v[74:75], 0, s[10:11]
	global_load_dwordx4 v[2:5], v66, s[8:9] nt
	global_load_dwordx4 v[6:9], v66, s[8:9] offset:1024 nt
	global_load_dwordx2 v[84:85], v[26:27], off nt
	global_load_dwordx2 v[86:87], v[26:27], off offset:512 nt
	global_load_dwordx2 v[88:89], v[26:27], off offset:1024 nt
	global_load_dwordx2 v[90:91], v[26:27], off offset:1536 nt
	global_load_dwordx4 v[10:13], v66, s[8:9] offset:2048 nt
	global_load_dwordx4 v[14:17], v66, s[8:9] offset:3072 nt
	global_load_dwordx4 v[18:21], v76, s[8:9] nt
	global_load_dwordx4 v[22:25], v78, s[8:9] nt
	global_load_dwordx2 v[92:93], v[26:27], off offset:2048 nt
	global_load_dwordx2 v[94:95], v[26:27], off offset:2560 nt
	global_load_dwordx2 v[96:97], v[26:27], off offset:3072 nt
	global_load_dwordx2 v[98:99], v[26:27], off offset:3584 nt
	s_nop 0
	global_load_dwordx4 v[26:29], v80, s[8:9] nt
	global_load_dwordx4 v[30:33], v82, s[8:9] nt
	s_lshl_b64 s[4:5], s[4:5], 2
	s_add_u32 s4, s17, s4
	s_addc_u32 s5, s20, s5
	s_add_u32 s8, s4, 0x4000
	s_addc_u32 s9, s5, 0
	s_add_u32 s56, s8, 0x1000
	s_addc_u32 s57, s9, 0
	s_add_u32 s10, s4, 0x8000
	s_addc_u32 s11, s5, 0
	s_add_u32 s38, s4, 0x6000
	s_addc_u32 s39, s5, 0
	v_mbcnt_lo_u32_b32 v244, -1, 0
	v_mbcnt_hi_u32_b32 v244, -1, v244
	v_lshlrev_b32_e32 v243, 4, v244
	v_readlane_b32 s4, v255, 1
	s_nop 4
	v_add_u32_e32 v244, s4, v244
	v_lshlrev_b32_e32 v244, 4, v244
	global_load_dwordx4 v[208:211], v244, s[14:15]
	global_load_dwordx4 v[212:215], v244, s[26:27]
	global_load_dwordx4 v[216:219], v244, s[10:11]
	s_add_u32 s4, s38, 0x1000
	s_addc_u32 s5, s39, 0
	v_add_u32_e32 v245, 0x20200, v244
	s_waitcnt vmcnt(0)
	ds_write_b128 v245, v[208:211]
	ds_write_b128 v245, v[212:215] offset:8192
	ds_write_b128 v245, v[216:219] offset:16384
	s_waitcnt lgkmcnt(0)
	global_load_dwordx4 v[208:211], v243, s[38:39]
	global_load_dwordx4 v[212:215], v243, s[38:39] offset:1024
	global_load_dwordx4 v[216:219], v243, s[38:39] offset:2048
	global_load_dwordx4 v[220:223], v243, s[38:39] offset:3072
	global_load_dwordx4 v[224:227], v243, s[4:5]
	global_load_dwordx4 v[228:231], v243, s[4:5] offset:1024
	global_load_dwordx4 v[232:235], v243, s[4:5] offset:2048
	global_load_dwordx4 v[236:239], v243, s[4:5] offset:3072
	s_nop 0
	v_add_u32_e32 v243, 0x20200, v243
	s_waitcnt vmcnt(0) lgkmcnt(0)
	s_barrier
	s_add_i32 s4, s33, s49
	s_ashr_i32 s5, s4, 31
	s_lshl_b64 s[40:41], s[4:5], 13
	s_add_u32 s40, s28, s40
	s_addc_u32 s41, s29, s41
	s_lshl_b64 s[4:5], s[4:5], 12
	v_lshl_add_u64 v[100:101], v[74:75], 0, s[4:5]
	v_lshl_add_u64 v[102:103], s[40:41], 0, v[66:67]
	v_lshl_add_u64 v[104:105], s[40:41], 0, v[76:77]
	v_lshl_add_u64 v[106:107], s[40:41], 0, v[78:79]
	v_lshl_add_u64 v[108:109], s[40:41], 0, v[80:81]
	v_lshl_add_u64 v[110:111], s[40:41], 0, v[82:83]
	s_mov_b64 s[4:5], -1
	s_mov_b32 s50, 0
	s_branch .LBB0_840
.LBB0_839:
	v_mov_b32_e32 v140, v149
	v_lshlrev_b32_e32 v166, 16, v126
	v_lshlrev_b32_e32 v128, 2, v140
	v_ashrrev_i32_e32 v129, 31, v128
	v_lshlrev_b64 v[130:131], 2, v[128:129]
	v_lshl_add_u64 v[146:147], s[8:9], 0, v[130:131]
	v_add_co_u32_e32 v146, vcc, s45, v146
	v_and_b32_e32 v167, 0xffff0000, v126
	s_nop 0
	v_addc_co_u32_e32 v147, vcc, 0, v147, vcc
	v_lshlrev_b32_e32 v168, 16, v127
	v_and_b32_e32 v169, 0xffff0000, v127
	v_lshlrev_b32_e32 v170, 16, v124
	v_and_b32_e32 v171, 0xffff0000, v124
	v_lshlrev_b32_e32 v172, 16, v125
	v_and_b32_e32 v173, 0xffff0000, v125
	v_lshlrev_b32_e32 v188, 16, v122
	v_and_b32_e32 v189, 0xffff0000, v122
	v_lshlrev_b32_e32 v190, 16, v123
	v_and_b32_e32 v191, 0xffff0000, v123
	v_lshlrev_b32_e32 v192, 16, v116
	v_and_b32_e32 v193, 0xffff0000, v116
	v_lshlrev_b32_e32 v194, 16, v117
	v_and_b32_e32 v195, 0xffff0000, v117
	v_lshlrev_b32_e32 v184, 16, v120
	v_and_b32_e32 v185, 0xffff0000, v120
	v_lshlrev_b32_e32 v120, 16, v121
	v_and_b32_e32 v121, 0xffff0000, v121
	v_lshlrev_b32_e32 v186, 16, v118
	v_and_b32_e32 v187, 0xffff0000, v118
	v_lshlrev_b32_e32 v118, 16, v119
	v_and_b32_e32 v119, 0xffff0000, v119
	s_mov_b32 s50, 2
	v_pk_add_f32 v[116:117], v[134:135], 1.0 op_sel_hi:[1,0]
	v_pk_add_f32 v[122:123], v[132:133], 1.0 op_sel_hi:[1,0]
	v_pk_add_f32 v[132:133], v[138:139], 1.0 op_sel_hi:[1,0]
	v_pk_add_f32 v[134:135], v[136:137], 1.0 op_sel_hi:[1,0]
	v_pk_add_f32 v[136:137], v[144:145], 1.0 op_sel_hi:[1,0]
	v_pk_add_f32 v[138:139], v[142:143], 1.0 op_sel_hi:[1,0]
	v_pk_mul_f32 v[122:123], v[122:123], v[166:167]
	v_pk_mul_f32 v[116:117], v[116:117], v[168:169]
	v_pk_add_f32 v[142:143], v[152:153], 1.0 op_sel_hi:[1,0]
	v_pk_add_f32 v[144:145], v[150:151], 1.0 op_sel_hi:[1,0]
	v_pk_mul_f32 v[134:135], v[134:135], v[170:171]
	v_pk_mul_f32 v[132:133], v[132:133], v[172:173]
	v_pk_mul_f32 v[146:147], v[138:139], v[184:185]
	v_pk_mul_f32 v[150:151], v[136:137], v[120:121]
	v_pk_add_f32 v[154:155], v[154:155], 1.0 op_sel_hi:[1,0]
	v_pk_fma_f32 v[136:137], v[52:53], s[36:37], v[116:117] op_sel_hi:[1,0,1]
	v_pk_fma_f32 v[138:139], v[50:51], s[36:37], v[122:123] op_sel_hi:[1,0,1]
	v_pk_mul_f32 v[142:143], v[142:143], v[118:119]
	v_pk_fma_f32 v[120:121], v[56:57], s[36:37], v[132:133] op_sel_hi:[1,0,1]
	v_pk_fma_f32 v[122:123], v[54:55], s[36:37], v[134:135] op_sel_hi:[1,0,1]
	v_pk_fma_f32 v[118:119], v[62:63], s[36:37], v[146:147] op_sel_hi:[1,0,1]
	v_pk_mul_f32 v[52:53], v[154:155], v[188:189]
	v_add_f32_e32 v62, v138, v139
	v_add_f32_e32 v63, v136, v137
	v_pk_mul_f32 v[144:145], v[144:145], v[186:187]
	v_pk_add_f32 v[152:153], v[156:157], 1.0 op_sel_hi:[1,0]
	v_pk_fma_f32 v[116:117], v[64:65], s[36:37], v[150:151] op_sel_hi:[1,0,1]
	v_add_f32_e32 v64, v122, v123
	v_add_f32_e32 v65, v120, v121
	v_pk_fma_f32 v[52:53], v[46:47], s[36:37], v[52:53] op_sel_hi:[1,0,1]
	v_add_f32_e32 v46, v62, v63
	v_pk_add_f32 v[156:157], v[160:161], 1.0 op_sel_hi:[1,0]
	v_pk_add_f32 v[158:159], v[158:159], 1.0 op_sel_hi:[1,0]
	v_pk_fma_f32 v[56:57], v[60:61], s[36:37], v[142:143] op_sel_hi:[1,0,1]
	v_pk_fma_f32 v[58:59], v[58:59], s[36:37], v[144:145] op_sel_hi:[1,0,1]
	v_pk_mul_f32 v[50:51], v[152:153], v[190:191]
	v_add_f32_e32 v132, v118, v119
	v_add_f32_e32 v133, v116, v117
	v_add_f32_e32 v47, v64, v65
	v_add_f32_e32 v46, 0, v46
	v_pk_mul_f32 v[54:55], v[156:157], v[194:195]
	v_pk_mul_f32 v[60:61], v[158:159], v[192:193]
	v_add_f32_e32 v134, v58, v59
	v_add_f32_e32 v135, v56, v57
	v_pk_fma_f32 v[50:51], v[48:49], s[36:37], v[50:51] op_sel_hi:[1,0,1]
	v_add_f32_e32 v48, v132, v133
	v_add_f32_e32 v46, v46, v47
	v_add_f32_e32 v49, v134, v135
	v_add_f32_e32 v62, v52, v53
	v_add_f32_e32 v63, v50, v51
	v_add_f32_e32 v46, v46, v48
	v_pk_fma_f32 v[44:45], v[44:45], s[36:37], v[54:55] op_sel_hi:[1,0,1]
	v_pk_fma_f32 v[42:43], v[42:43], s[36:37], v[60:61] op_sel_hi:[1,0,1]
	v_add_f32_e32 v62, v62, v63
	v_add_f32_e32 v46, v46, v49
	v_add_f32_e32 v47, v42, v43
	v_add_f32_e32 v48, v44, v45
	v_add_f32_e32 v46, v46, v62
	v_add_f32_e32 v47, v47, v48
	v_add_f32_e32 v62, v46, v47
	v_lshlrev_b32_e32 v46, 16, v114
	v_and_b32_e32 v47, 0xffff0000, v114
	v_lshlrev_b32_e32 v48, 16, v115
	v_and_b32_e32 v49, 0xffff0000, v115
	v_pk_add_f32 v[54:55], v[246:247], 1.0 op_sel_hi:[1,0]
	v_pk_add_f32 v[60:61], v[244:245], 1.0 op_sel_hi:[1,0]
	v_pk_mul_f32 v[48:49], v[54:55], v[48:49]
	v_pk_mul_f32 v[46:47], v[60:61], v[46:47]
	v_pk_fma_f32 v[40:41], v[40:41], s[36:37], v[48:49] op_sel_hi:[1,0,1]
	v_pk_fma_f32 v[38:39], v[38:39], s[36:37], v[46:47] op_sel_hi:[1,0,1]
	v_add_f32_e32 v47, v40, v41
	v_add_f32_e32 v46, v38, v39
	v_add_f32_e32 v46, v46, v47
	v_add_f32_e32 v62, v62, v46
	v_lshlrev_b32_e32 v46, 16, v112
	v_and_b32_e32 v47, 0xffff0000, v112
	v_lshlrev_b32_e32 v48, 16, v113
	v_and_b32_e32 v49, 0xffff0000, v113
	v_pk_add_f32 v[54:55], v[164:165], 1.0 op_sel_hi:[1,0]
	v_pk_add_f32 v[60:61], v[162:163], 1.0 op_sel_hi:[1,0]
	v_pk_mul_f32 v[48:49], v[54:55], v[48:49]
	v_pk_mul_f32 v[46:47], v[60:61], v[46:47]
	v_pk_fma_f32 v[36:37], v[36:37], s[36:37], v[48:49] op_sel_hi:[1,0,1]
	v_pk_fma_f32 v[34:35], v[34:35], s[36:37], v[46:47] op_sel_hi:[1,0,1]
	v_add_f32_e32 v47, v36, v37
	v_add_f32_e32 v46, v34, v35
	v_add_f32_e32 v46, v46, v47
	v_add_f32_e32 v46, v62, v46
	v_lshl_add_u64 v[134:135], s[14:15], 0, v[130:131]
	v_lshl_add_u64 v[132:133], s[26:27], 0, v[130:131]
	v_add_f32_dpp v46, v46, v46 quad_perm:[1,0,3,2] row_mask:0xf bank_mask:0xf bound_ctrl:1
	v_lshl_add_u64 v[126:127], s[10:11], 0, v[130:131]
	v_lshl_add_u64 v[124:125], s[38:39], 0, v[130:131]
	v_add_f32_dpp v46, v46, v46 quad_perm:[2,3,0,1] row_mask:0xf bank_mask:0xf bound_ctrl:1
	s_nop 1
	v_add_f32_dpp v46, v46, v46 row_half_mirror row_mask:0xf bank_mask:0xf bound_ctrl:1
	s_nop 1
	v_add_f32_dpp v46, v46, v46 row_mirror row_mask:0xf bank_mask:0xf bound_ctrl:1
	v_mov_b32_e32 v47, v46
	s_nop 1
	v_permlane16_swap_b32_e32 v46, v47
	v_add_f32_e32 v46, v46, v47
	v_mov_b32_e32 v47, v46
	s_nop 1
	v_permlane32_swap_b32_e32 v46, v47
	v_add_f32_e32 v46, v46, v47
	v_fmac_f32_e32 v137, 0xba000000, v46
	v_fmac_f32_e32 v139, 0xba000000, v46
	v_fmamk_f32 v136, v46, 0xba000000, v136
	v_fmamk_f32 v138, v46, 0xba000000, v138
	v_mul_f32_e32 v47, v139, v139
	v_mul_f32_e32 v48, v137, v137
	v_fmac_f32_e32 v47, v138, v138
	v_fmac_f32_e32 v48, v136, v136
	v_fmac_f32_e32 v121, 0xba000000, v46
	v_fmac_f32_e32 v123, 0xba000000, v46
	v_add_f32_e32 v47, v47, v48
	v_fmamk_f32 v120, v46, 0xba000000, v120
	v_fmamk_f32 v122, v46, 0xba000000, v122
	v_mul_f32_e32 v48, v123, v123
	v_mul_f32_e32 v49, v121, v121
	v_fmac_f32_e32 v48, v122, v122
	v_fmac_f32_e32 v49, v120, v120
	v_add_f32_e32 v48, v48, v49
	v_fmac_f32_e32 v117, 0xba000000, v46
	v_fmac_f32_e32 v119, 0xba000000, v46
	v_add_f32_e32 v47, v47, v48
	v_fmamk_f32 v116, v46, 0xba000000, v116
	v_fmamk_f32 v118, v46, 0xba000000, v118
	v_mul_f32_e32 v48, v119, v119
	v_mul_f32_e32 v49, v117, v117
	v_fmac_f32_e32 v48, v118, v118
	v_fmac_f32_e32 v49, v116, v116
	v_add_f32_e32 v48, v48, v49
	v_fmac_f32_e32 v57, 0xba000000, v46
	v_fmac_f32_e32 v59, 0xba000000, v46
	v_add_f32_e32 v47, v48, v47
	v_fmamk_f32 v56, v46, 0xba000000, v56
	v_fmamk_f32 v58, v46, 0xba000000, v58
	v_mul_f32_e32 v48, v59, v59
	v_mul_f32_e32 v49, v57, v57
	v_fmac_f32_e32 v48, v58, v58
	v_fmac_f32_e32 v49, v56, v56
	v_add_f32_e32 v48, v48, v49
	v_fmac_f32_e32 v51, 0xba000000, v46
	v_fmac_f32_e32 v53, 0xba000000, v46
	v_add_f32_e32 v47, v48, v47
	v_fmamk_f32 v50, v46, 0xba000000, v50
	v_fmamk_f32 v52, v46, 0xba000000, v52
	v_mul_f32_e32 v48, v53, v53
	v_mul_f32_e32 v49, v51, v51
	v_fmac_f32_e32 v48, v52, v52
	v_fmac_f32_e32 v49, v50, v50
	v_add_f32_e32 v48, v48, v49
	v_fmac_f32_e32 v45, 0xba000000, v46
	v_fmac_f32_e32 v43, 0xba000000, v46
	v_add_f32_e32 v47, v48, v47
	v_fmamk_f32 v44, v46, 0xba000000, v44
	v_fmamk_f32 v42, v46, 0xba000000, v42
	v_mul_f32_e32 v48, v43, v43
	v_mul_f32_e32 v49, v45, v45
	v_fmac_f32_e32 v48, v42, v42
	v_fmac_f32_e32 v49, v44, v44
	v_add_f32_e32 v48, v48, v49
	v_fmac_f32_e32 v41, 0xba000000, v46
	v_fmac_f32_e32 v39, 0xba000000, v46
	v_add_f32_e32 v47, v48, v47
	v_fmamk_f32 v40, v46, 0xba000000, v40
	v_fmamk_f32 v38, v46, 0xba000000, v38
	v_mul_f32_e32 v48, v39, v39
	v_mul_f32_e32 v49, v41, v41
	v_fmac_f32_e32 v48, v38, v38
	v_fmac_f32_e32 v49, v40, v40
	v_add_f32_e32 v48, v48, v49
	v_fmac_f32_e32 v37, 0xba000000, v46
	v_fmac_f32_e32 v35, 0xba000000, v46
	v_add_f32_e32 v47, v48, v47
	v_fmamk_f32 v36, v46, 0xba000000, v36
	v_fmamk_f32 v34, v46, 0xba000000, v34
	v_mul_f32_e32 v46, v35, v35
	v_mul_f32_e32 v48, v37, v37
	v_fmac_f32_e32 v46, v34, v34
	v_fmac_f32_e32 v48, v36, v36
	v_add_f32_e32 v46, v46, v48
	v_add_f32_e32 v46, v46, v47
	s_nop 1
	v_add_f32_dpp v46, v46, v46 quad_perm:[1,0,3,2] row_mask:0xf bank_mask:0xf bound_ctrl:1
	s_nop 1
	v_add_f32_dpp v46, v46, v46 quad_perm:[2,3,0,1] row_mask:0xf bank_mask:0xf bound_ctrl:1
	s_nop 1
	v_add_f32_dpp v46, v46, v46 row_half_mirror row_mask:0xf bank_mask:0xf bound_ctrl:1
	s_nop 1
	v_add_f32_dpp v46, v46, v46 row_mirror row_mask:0xf bank_mask:0xf bound_ctrl:1
	v_mov_b32_e32 v47, v46
	s_nop 1
	v_permlane16_swap_b32_e32 v46, v47
	v_add_f32_e32 v54, v46, v47
	v_mov_b32_e32 v55, v54
	ds_read_b128 v[46:49], v243 offset:0
	ds_read_b128 v[60:63], v243 offset:8192
	ds_read_b128 v[112:115], v243 offset:16384
	v_mov_b32_e32 v142, v208
	v_mov_b32_e32 v143, v209
	v_mov_b32_e32 v144, v210
	v_mov_b32_e32 v145, v211
	v_permlane32_swap_b32_e32 v54, v55
	v_add_f32_e32 v54, v54, v55
	v_fmamk_f32 v54, v54, 0x3a000000, v176
	v_mul_f32_e32 v55, 0x4f800000, v54
	v_cmp_gt_f32_e32 vcc, s46, v54
	s_nop 1
	v_cndmask_b32_e32 v54, v54, v55, vcc
	v_sqrt_f32_e32 v55, v54
	s_nop 0
	v_add_u32_e32 v64, -1, v55
	v_fma_f32 v65, -v64, v55, v54
	v_cmp_ge_f32_e64 s[4:5], 0, v65
	v_add_u32_e32 v65, 1, v55
	s_nop 0
	v_cndmask_b32_e64 v64, v55, v64, s[4:5]
	v_fma_f32 v55, -v65, v55, v54
	v_cmp_lt_f32_e64 s[4:5], 0, v55
	s_nop 1
	v_cndmask_b32_e64 v55, v64, v65, s[4:5]
	v_mul_f32_e32 v64, 0x37800000, v55
	v_cndmask_b32_e32 v55, v55, v64, vcc
	v_cmp_class_f32_e32 vcc, v54, v177
	s_nop 1
	v_cndmask_b32_e32 v54, v55, v54, vcc
	v_div_scale_f32 v55, s[4:5], v54, v54, 1.0
	v_rcp_f32_e32 v64, v55
	s_lshl_b64 s[4:5], s[42:43], 1
	s_add_u32 s4, s21, s4
	s_addc_u32 s5, s22, s5
	v_fma_f32 v65, -v55, v64, 1.0
	v_fmac_f32_e32 v64, v65, v64
	v_div_scale_f32 v65, vcc, 1.0, v54, 1.0
	v_mul_f32_e32 v130, v65, v64
	v_fma_f32 v131, -v55, v130, v65
	v_fmac_f32_e32 v130, v131, v64
	v_fma_f32 v55, -v55, v130, v65
	v_div_fmas_f32 v55, v55, v64, v130
	v_div_fixup_f32 v54, v55, v54, 1.0
	v_pk_mul_f32 v[64:65], v[138:139], v[54:55] op_sel_hi:[1,0]
	v_pk_mul_f32 v[130:131], v[136:137], v[54:55] op_sel_hi:[1,0]
	s_add_u32 s42, s23, s42
	s_addc_u32 s43, s24, s43
	s_or_b32 s7, s7, s25
	s_mulk_i32 s7, 0x1010
	s_add_i32 s7, s7, 0
	v_lshl_add_u32 v146, v140, 3, s7
	s_waitcnt lgkmcnt(0)
	v_pk_fma_f32 v[46:47], v[46:47], v[64:65], v[60:61]
	s_nop 0
	v_bfe_u32 v55, v46, 16, 1
	v_add3_u32 v55, v46, v55, s47
	v_bfe_u32 v60, v47, 16, 1
	v_pk_fma_f32 v[48:49], v[48:49], v[130:131], v[62:63]
	v_lshrrev_b32_e32 v55, 16, v55
	v_add3_u32 v60, v47, v60, s47
	v_and_or_b32 v64, v60, s44, v55
	v_bfe_u32 v60, v49, 16, 1
	v_add3_u32 v62, v49, v60, s47
	v_pk_add_f32 v[60:61], v[112:113], 1.0 op_sel_hi:[1,0]
	v_mov_b32_e32 v112, 0
	v_pk_fma_f32 v[60:61], v[60:61], v[46:47], v[142:143]
	v_bfe_u32 v55, v48, 16, 1
	v_cvt_pk_fp8_f32 v112, v60, v61
	v_add3_u32 v55, v48, v55, s47
	v_lshrrev_b32_e32 v55, 16, v55
	v_pk_add_f32 v[46:47], v[114:115], 1.0 op_sel_hi:[1,0]
	v_and_or_b32 v65, v62, s44, v55
	v_pk_fma_f32 v[62:63], v[46:47], v[48:49], v[144:145]
	v_lshl_add_u64 v[48:49], v[128:129], 1, s[4:5]
	v_cvt_pk_fp8_f32 v112, v62, v63 op_sel:[0,0,1]
	v_lshl_add_u64 v[46:47], s[42:43], 0, v[128:129]
	global_store_dwordx2 v[48:49], v[64:65], off
	v_pk_mul_f32 v[64:65], v[122:123], v[54:55] op_sel_hi:[1,0]
	global_store_dword v[46:47], v112, off
	ds_read_b128 v[112:115], v243 offset:1024
	s_nop 0
	ds_read_b128 v[128:131], v243 offset:9216
	ds_read_b128 v[136:139], v243 offset:17408
	v_mov_b32_e32 v142, v212
	v_mov_b32_e32 v143, v213
	v_mov_b32_e32 v144, v214
	v_mov_b32_e32 v145, v215
	v_pk_mul_f32 v[120:121], v[120:121], v[54:55] op_sel_hi:[1,0]
	v_mov_b32_e32 v122, 0
	s_mov_b64 s[4:5], 0
	s_waitcnt lgkmcnt(0)
	v_pk_fma_f32 v[64:65], v[112:113], v[64:65], v[128:129]
	s_nop 0
	v_bfe_u32 v55, v64, 16, 1
	v_add3_u32 v55, v64, v55, s47
	v_bfe_u32 v112, v65, 16, 1
	v_lshrrev_b32_e32 v55, 16, v55
	v_add3_u32 v112, v65, v112, s47
	v_pk_fma_f32 v[114:115], v[114:115], v[120:121], v[130:131]
	v_and_or_b32 v120, v112, s44, v55
	v_pk_add_f32 v[112:113], v[136:137], 1.0 op_sel_hi:[1,0]
	v_bfe_u32 v55, v114, 16, 1
	v_pk_fma_f32 v[64:65], v[64:65], v[112:113], v[142:143]
	v_pk_add_f32 v[112:113], v[138:139], 1.0 op_sel_hi:[1,0]
	v_cvt_pk_fp8_f32 v122, v64, v65
	v_pk_fma_f32 v[112:113], v[114:115], v[112:113], v[144:145]
	v_add3_u32 v55, v114, v55, s47
	v_bfe_u32 v121, v115, 16, 1
	v_cvt_pk_fp8_f32 v122, v112, v113 op_sel:[0,0,1]
	v_lshrrev_b32_e32 v55, 16, v55
	v_add3_u32 v114, v115, v121, s47
	v_and_or_b32 v121, v114, s44, v55
	global_store_dwordx2 v[48:49], v[120:121], off offset:512
	global_store_dword v[46:47], v122, off offset:256
	ds_read_b128 v[120:123], v243 offset:2048
	s_nop 0
	ds_read_b128 v[128:131], v243 offset:10240
	ds_read_b128 v[136:139], v243 offset:18432
	v_mov_b32_e32 v142, v216
	v_mov_b32_e32 v143, v217
	v_mov_b32_e32 v144, v218
	v_mov_b32_e32 v145, v219
	v_mov_b32_e32 v55, 0
	v_pk_mul_f32 v[114:115], v[118:119], v[54:55] op_sel_hi:[1,0]
	v_pk_mul_f32 v[116:117], v[116:117], v[54:55] op_sel_hi:[1,0]
	s_waitcnt lgkmcnt(0)
	v_pk_fma_f32 v[120:121], v[114:115], v[120:121], v[128:129]
	v_pk_fma_f32 v[118:119], v[116:117], v[122:123], v[130:131]
	v_pk_add_f32 v[116:117], v[136:137], 1.0 op_sel_hi:[1,0]
	v_pk_add_f32 v[114:115], v[138:139], 1.0 op_sel_hi:[1,0]
	v_pk_fma_f32 v[116:117], v[120:121], v[116:117], v[142:143]
	v_bfe_u32 v122, v120, 16, 1
	v_cvt_pk_fp8_f32 v55, v116, v117
	v_bfe_u32 v128, v118, 16, 1
	v_pk_fma_f32 v[114:115], v[118:119], v[114:115], v[144:145]
	v_bfe_u32 v123, v121, 16, 1
	v_bfe_u32 v129, v119, 16, 1
	v_add3_u32 v120, v120, v122, s47
	v_add3_u32 v118, v118, v128, s47
	v_cvt_pk_fp8_f32 v55, v114, v115 op_sel:[0,0,1]
	v_add3_u32 v121, v121, v123, s47
	v_add3_u32 v119, v119, v129, s47
	v_lshrrev_b32_e32 v120, 16, v120
	v_lshrrev_b32_e32 v122, 16, v118
	v_and_or_b32 v118, v121, s44, v120
	v_and_or_b32 v119, v119, s44, v122
	global_store_dwordx2 v[48:49], v[118:119], off offset:1024
	global_store_dword v[46:47], v55, off offset:512
	ds_read_b128 v[128:131], v243 offset:3072
	ds_read_b128 v[136:139], v243 offset:11264
	ds_read_b128 v[142:145], v243 offset:19456
	v_mov_b32_e32 v150, v220
	v_mov_b32_e32 v151, v221
	v_mov_b32_e32 v152, v222
	v_mov_b32_e32 v153, v223
	v_mov_b32_e32 v55, 0
	v_pk_mul_f32 v[58:59], v[58:59], v[54:55] op_sel_hi:[1,0]
	v_pk_mul_f32 v[56:57], v[56:57], v[54:55] op_sel_hi:[1,0]
	v_add_co_u32_e32 v118, vcc, s45, v134
	s_waitcnt lgkmcnt(0)
	v_pk_fma_f32 v[128:129], v[58:59], v[128:129], v[136:137]
	v_pk_add_f32 v[58:59], v[142:143], 1.0 op_sel_hi:[1,0]
	v_addc_co_u32_e32 v119, vcc, 0, v135, vcc
	v_pk_fma_f32 v[58:59], v[128:129], v[58:59], v[150:151]
	v_pk_fma_f32 v[122:123], v[56:57], v[130:131], v[138:139]
	v_cvt_pk_fp8_f32 v55, v58, v59
	v_pk_add_f32 v[56:57], v[144:145], 1.0 op_sel_hi:[1,0]
	v_add_co_u32_e32 v120, vcc, s45, v132
	v_bfe_u32 v130, v128, 16, 1
	v_bfe_u32 v132, v122, 16, 1
	v_pk_fma_f32 v[56:57], v[122:123], v[56:57], v[152:153]
	v_addc_co_u32_e32 v121, vcc, 0, v133, vcc
	v_bfe_u32 v131, v129, 16, 1
	v_bfe_u32 v133, v123, 16, 1
	v_add3_u32 v128, v128, v130, s47
	v_add3_u32 v122, v122, v132, s47
	v_cvt_pk_fp8_f32 v55, v56, v57 op_sel:[0,0,1]
	v_add3_u32 v129, v129, v131, s47
	v_add3_u32 v123, v123, v133, s47
	v_lshrrev_b32_e32 v128, 16, v128
	v_lshrrev_b32_e32 v130, 16, v122
	v_add_co_u32_e32 v126, vcc, s45, v126
	v_and_or_b32 v122, v129, s44, v128
	v_and_or_b32 v123, v123, s44, v130
	v_addc_co_u32_e32 v127, vcc, 0, v127, vcc
	global_store_dwordx2 v[48:49], v[122:123], off offset:1536
	global_store_dword v[46:47], v55, off offset:768
	v_add_co_u32_e32 v122, vcc, s45, v124
	ds_read_b128 v[128:131], v243 offset:4096
	ds_read_b128 v[132:135], v243 offset:12288
	ds_read_b128 v[136:139], v243 offset:20480
	v_addc_co_u32_e32 v123, vcc, 0, v125, vcc
	v_mov_b32_e32 v142, v224
	v_mov_b32_e32 v143, v225
	v_mov_b32_e32 v144, v226
	v_mov_b32_e32 v145, v227
	v_mov_b32_e32 v55, 0
	v_pk_mul_f32 v[52:53], v[52:53], v[54:55] op_sel_hi:[1,0]
	v_pk_mul_f32 v[50:51], v[50:51], v[54:55] op_sel_hi:[1,0]
	s_and_b64 vcc, exec, s[40:41]
	s_waitcnt lgkmcnt(0)
	v_pk_fma_f32 v[128:129], v[52:53], v[128:129], v[132:133]
	v_pk_add_f32 v[52:53], v[136:137], 1.0 op_sel_hi:[1,0]
	v_pk_fma_f32 v[124:125], v[50:51], v[130:131], v[134:135]
	v_pk_add_f32 v[50:51], v[138:139], 1.0 op_sel_hi:[1,0]
	v_pk_fma_f32 v[52:53], v[128:129], v[52:53], v[142:143]
	v_bfe_u32 v130, v128, 16, 1
	v_cvt_pk_fp8_f32 v55, v52, v53
	v_bfe_u32 v132, v124, 16, 1
	v_pk_fma_f32 v[50:51], v[124:125], v[50:51], v[144:145]
	v_bfe_u32 v131, v129, 16, 1
	v_bfe_u32 v133, v125, 16, 1
	v_add3_u32 v128, v128, v130, s47
	v_add3_u32 v124, v124, v132, s47
	v_cvt_pk_fp8_f32 v55, v50, v51 op_sel:[0,0,1]
	v_add3_u32 v129, v129, v131, s47
	v_add3_u32 v125, v125, v133, s47
	v_lshrrev_b32_e32 v128, 16, v128
	v_lshrrev_b32_e32 v130, 16, v124
	v_and_or_b32 v124, v129, s44, v128
	v_and_or_b32 v125, v125, s44, v130
	global_store_dwordx2 v[48:49], v[124:125], off offset:2048
	global_store_dword v[46:47], v55, off offset:1024
	ds_read_b128 v[128:131], v243 offset:5120
	ds_read_b128 v[132:135], v243 offset:13312
	ds_read_b128 v[136:139], v243 offset:21504
	v_mov_b32_e32 v142, v228
	v_mov_b32_e32 v143, v229
	v_mov_b32_e32 v144, v230
	v_mov_b32_e32 v145, v231
	v_mov_b32_e32 v55, 0
	v_pk_mul_f32 v[42:43], v[42:43], v[54:55] op_sel_hi:[1,0]
	v_pk_mul_f32 v[44:45], v[44:45], v[54:55] op_sel_hi:[1,0]
	s_waitcnt lgkmcnt(0)
	v_pk_fma_f32 v[42:43], v[42:43], v[128:129], v[132:133]
	v_pk_add_f32 v[128:129], v[136:137], 1.0 op_sel_hi:[1,0]
	v_pk_fma_f32 v[44:45], v[44:45], v[130:131], v[134:135]
	v_pk_fma_f32 v[142:143], v[42:43], v[128:129], v[142:143]
	v_pk_add_f32 v[124:125], v[138:139], 1.0 op_sel_hi:[1,0]
	v_cvt_pk_fp8_f32 v55, v142, v143
	v_bfe_u32 v130, v42, 16, 1
	v_bfe_u32 v132, v44, 16, 1
	v_pk_fma_f32 v[124:125], v[44:45], v[124:125], v[144:145]
	v_bfe_u32 v131, v43, 16, 1
	v_bfe_u32 v133, v45, 16, 1
	v_add3_u32 v42, v42, v130, s47
	v_add3_u32 v44, v44, v132, s47
	v_cvt_pk_fp8_f32 v55, v124, v125 op_sel:[0,0,1]
	v_add3_u32 v43, v43, v131, s47
	v_add3_u32 v45, v45, v133, s47
	v_lshrrev_b32_e32 v42, 16, v42
	v_lshrrev_b32_e32 v44, 16, v44
	v_and_or_b32 v42, v43, s44, v42
	v_and_or_b32 v43, v45, s44, v44
	global_store_dwordx2 v[48:49], v[42:43], off offset:2560
	global_store_dword v[46:47], v55, off offset:1280
	ds_read_b128 v[42:45], v243 offset:6144
	s_nop 0
	ds_read_b128 v[128:131], v243 offset:14336
	ds_read_b128 v[132:135], v243 offset:22528
	v_mov_b32_e32 v136, v232
	v_mov_b32_e32 v137, v233
	v_mov_b32_e32 v138, v234
	v_mov_b32_e32 v139, v235
	v_pk_mul_f32 v[38:39], v[38:39], v[54:55] op_sel_hi:[1,0]
	v_pk_mul_f32 v[40:41], v[40:41], v[54:55] op_sel_hi:[1,0]
	v_pk_mul_f32 v[140:141], v[34:35], v[54:55] op_sel_hi:[1,0]
	v_pk_mul_f32 v[54:55], v[36:37], v[54:55] op_sel_hi:[1,0]
	v_and_b32_sdwa v34, v62, v182 dst_sel:DWORD dst_unused:UNUSED_PAD src0_sel:WORD_1 src1_sel:DWORD
	v_and_b32_sdwa v35, v60, v182 dst_sel:DWORD dst_unused:UNUSED_PAD src0_sel:WORD_1 src1_sel:DWORD
	v_and_b32_sdwa v36, v63, v182 dst_sel:DWORD dst_unused:UNUSED_PAD src0_sel:WORD_1 src1_sel:DWORD
	v_and_b32_sdwa v37, v61, v182 dst_sel:DWORD dst_unused:UNUSED_PAD src0_sel:WORD_1 src1_sel:DWORD
	v_add3_u32 v60, v60, v35, s47
	v_add3_u32 v62, v62, v34, s47
	v_add3_u32 v34, v63, v36, s47
	v_add3_u32 v35, v61, v37, s47
	v_and_b32_e32 v61, 0xffff0000, v34
	v_and_b32_e32 v63, 0xffff0000, v35
	v_mov_b32_e32 v144, 0
	v_mov_b32_e32 v145, 0
	s_waitcnt lgkmcnt(0)
	v_pk_fma_f32 v[34:35], v[40:41], v[44:45], v[130:131]
	v_pk_fma_f32 v[36:37], v[38:39], v[42:43], v[128:129]
	v_pk_add_f32 v[40:41], v[132:133], 1.0 op_sel_hi:[1,0]
	v_pk_add_f32 v[38:39], v[134:135], 1.0 op_sel_hi:[1,0]
	v_pk_fma_f32 v[130:131], v[36:37], v[40:41], v[136:137]
	v_bfe_u32 v42, v36, 16, 1
	v_cvt_pk_fp8_f32 v144, v130, v131
	v_bfe_u32 v44, v34, 16, 1
	v_pk_fma_f32 v[128:129], v[34:35], v[38:39], v[138:139]
	v_bfe_u32 v43, v37, 16, 1
	v_bfe_u32 v45, v35, 16, 1
	v_add3_u32 v36, v36, v42, s47
	v_add3_u32 v34, v34, v44, s47
	v_cvt_pk_fp8_f32 v144, v128, v129 op_sel:[0,0,1]
	v_add3_u32 v37, v37, v43, s47
	v_add3_u32 v35, v35, v45, s47
	v_lshrrev_b32_e32 v36, 16, v36
	v_lshrrev_b32_e32 v38, 16, v34
	v_and_or_b32 v34, v37, s44, v36
	v_and_or_b32 v35, v35, s44, v38
	global_store_dwordx2 v[48:49], v[34:35], off offset:3072
	global_store_dword v[46:47], v144, off offset:1536
	ds_read_b128 v[34:37], v243 offset:7168
	s_nop 0
	ds_read_b128 v[38:41], v243 offset:15360
	ds_read_b128 v[42:45], v243 offset:23552
	v_or_b32_sdwa v119, v61, v62 dst_sel:DWORD dst_unused:UNUSED_PAD src0_sel:DWORD src1_sel:WORD_1
	v_or_b32_sdwa v118, v63, v60 dst_sel:DWORD dst_unused:UNUSED_PAD src0_sel:DWORD src1_sel:WORD_1
	v_mov_b32_e32 v60, v236
	v_mov_b32_e32 v61, v237
	v_mov_b32_e32 v62, v238
	v_mov_b32_e32 v63, v239
	v_and_b32_sdwa v126, v113, v182 dst_sel:DWORD dst_unused:UNUSED_PAD src0_sel:WORD_1 src1_sel:DWORD
	v_and_b32_sdwa v127, v65, v182 dst_sel:DWORD dst_unused:UNUSED_PAD src0_sel:WORD_1 src1_sel:DWORD
	v_and_b32_sdwa v120, v112, v182 dst_sel:DWORD dst_unused:UNUSED_PAD src0_sel:WORD_1 src1_sel:DWORD
	v_and_b32_sdwa v121, v64, v182 dst_sel:DWORD dst_unused:UNUSED_PAD src0_sel:WORD_1 src1_sel:DWORD
	v_add3_u32 v113, v113, v126, s47
	v_add3_u32 v65, v65, v127, s47
	v_add3_u32 v64, v64, v121, s47
	v_add3_u32 v112, v112, v120, s47
	v_and_b32_e32 v113, 0xffff0000, v113
	v_and_b32_e32 v120, 0xffff0000, v65
	v_or_b32_sdwa v65, v113, v112 dst_sel:DWORD dst_unused:UNUSED_PAD src0_sel:DWORD src1_sel:WORD_1
	v_or_b32_sdwa v64, v120, v64 dst_sel:DWORD dst_unused:UNUSED_PAD src0_sel:DWORD src1_sel:WORD_1
	ds_write2st64_b64 v146, v[118:119], v[64:65] offset1:1
	v_and_b32_sdwa v65, v116, v182 dst_sel:DWORD dst_unused:UNUSED_PAD src0_sel:WORD_1 src1_sel:DWORD
	v_and_b32_sdwa v112, v115, v182 dst_sel:DWORD dst_unused:UNUSED_PAD src0_sel:WORD_1 src1_sel:DWORD
	v_and_b32_sdwa v113, v117, v182 dst_sel:DWORD dst_unused:UNUSED_PAD src0_sel:WORD_1 src1_sel:DWORD
	v_and_b32_sdwa v64, v114, v182 dst_sel:DWORD dst_unused:UNUSED_PAD src0_sel:WORD_1 src1_sel:DWORD
	v_add3_u32 v116, v116, v65, s47
	v_add3_u32 v65, v115, v112, s47
	v_add3_u32 v112, v117, v113, s47
	v_add3_u32 v64, v114, v64, s47
	v_and_b32_e32 v65, 0xffff0000, v65
	v_and_b32_e32 v112, 0xffff0000, v112
	v_and_b32_sdwa v114, v57, v182 dst_sel:DWORD dst_unused:UNUSED_PAD src0_sel:WORD_1 src1_sel:DWORD
	v_and_b32_sdwa v115, v59, v182 dst_sel:DWORD dst_unused:UNUSED_PAD src0_sel:WORD_1 src1_sel:DWORD
	v_or_b32_sdwa v65, v65, v64 dst_sel:DWORD dst_unused:UNUSED_PAD src0_sel:DWORD src1_sel:WORD_1
	v_or_b32_sdwa v64, v112, v116 dst_sel:DWORD dst_unused:UNUSED_PAD src0_sel:DWORD src1_sel:WORD_1
	v_and_b32_sdwa v112, v56, v182 dst_sel:DWORD dst_unused:UNUSED_PAD src0_sel:WORD_1 src1_sel:DWORD
	v_and_b32_sdwa v113, v58, v182 dst_sel:DWORD dst_unused:UNUSED_PAD src0_sel:WORD_1 src1_sel:DWORD
	v_add3_u32 v57, v57, v114, s47
	v_add3_u32 v59, v59, v115, s47
	v_add3_u32 v58, v58, v113, s47
	v_add3_u32 v56, v56, v112, s47
	v_and_b32_e32 v57, 0xffff0000, v57
	v_and_b32_e32 v59, 0xffff0000, v59
	v_or_b32_sdwa v57, v57, v56 dst_sel:DWORD dst_unused:UNUSED_PAD src0_sel:DWORD src1_sel:WORD_1
	v_or_b32_sdwa v56, v59, v58 dst_sel:DWORD dst_unused:UNUSED_PAD src0_sel:DWORD src1_sel:WORD_1
	v_and_b32_sdwa v58, v51, v182 dst_sel:DWORD dst_unused:UNUSED_PAD src0_sel:WORD_1 src1_sel:DWORD
	v_and_b32_sdwa v59, v53, v182 dst_sel:DWORD dst_unused:UNUSED_PAD src0_sel:WORD_1 src1_sel:DWORD
	ds_write2st64_b64 v146, v[64:65], v[56:57] offset0:2 offset1:3
	v_and_b32_sdwa v56, v50, v182 dst_sel:DWORD dst_unused:UNUSED_PAD src0_sel:WORD_1 src1_sel:DWORD
	v_and_b32_sdwa v57, v52, v182 dst_sel:DWORD dst_unused:UNUSED_PAD src0_sel:WORD_1 src1_sel:DWORD
	v_add3_u32 v51, v51, v58, s47
	v_add3_u32 v53, v53, v59, s47
	v_add3_u32 v52, v52, v57, s47
	v_add3_u32 v50, v50, v56, s47
	v_and_b32_e32 v51, 0xffff0000, v51
	v_and_b32_e32 v53, 0xffff0000, v53
	v_or_b32_sdwa v51, v51, v50 dst_sel:DWORD dst_unused:UNUSED_PAD src0_sel:DWORD src1_sel:WORD_1
	v_or_b32_sdwa v50, v53, v52 dst_sel:DWORD dst_unused:UNUSED_PAD src0_sel:DWORD src1_sel:WORD_1
	v_and_b32_sdwa v53, v142, v182 dst_sel:DWORD dst_unused:UNUSED_PAD src0_sel:WORD_1 src1_sel:DWORD
	v_and_b32_sdwa v56, v125, v182 dst_sel:DWORD dst_unused:UNUSED_PAD src0_sel:WORD_1 src1_sel:DWORD
	v_and_b32_sdwa v57, v143, v182 dst_sel:DWORD dst_unused:UNUSED_PAD src0_sel:WORD_1 src1_sel:DWORD
	v_and_b32_sdwa v52, v124, v182 dst_sel:DWORD dst_unused:UNUSED_PAD src0_sel:WORD_1 src1_sel:DWORD
	v_add3_u32 v58, v142, v53, s47
	v_add3_u32 v53, v125, v56, s47
	v_add3_u32 v56, v143, v57, s47
	v_add3_u32 v52, v124, v52, s47
	v_and_b32_e32 v53, 0xffff0000, v53
	v_and_b32_e32 v56, 0xffff0000, v56
	v_or_b32_sdwa v53, v53, v52 dst_sel:DWORD dst_unused:UNUSED_PAD src0_sel:DWORD src1_sel:WORD_1
	v_or_b32_sdwa v52, v56, v58 dst_sel:DWORD dst_unused:UNUSED_PAD src0_sel:DWORD src1_sel:WORD_1
	ds_write2st64_b64 v146, v[50:51], v[52:53] offset0:4 offset1:5
	v_and_b32_sdwa v51, v130, v182 dst_sel:DWORD dst_unused:UNUSED_PAD src0_sel:WORD_1 src1_sel:DWORD
	v_and_b32_sdwa v52, v129, v182 dst_sel:DWORD dst_unused:UNUSED_PAD src0_sel:WORD_1 src1_sel:DWORD
	v_and_b32_sdwa v53, v131, v182 dst_sel:DWORD dst_unused:UNUSED_PAD src0_sel:WORD_1 src1_sel:DWORD
	v_and_b32_sdwa v50, v128, v182 dst_sel:DWORD dst_unused:UNUSED_PAD src0_sel:WORD_1 src1_sel:DWORD
	v_add3_u32 v56, v130, v51, s47
	v_add3_u32 v51, v129, v52, s47
	v_add3_u32 v52, v131, v53, s47
	v_add3_u32 v50, v128, v50, s47
	v_and_b32_e32 v51, 0xffff0000, v51
	v_and_b32_e32 v52, 0xffff0000, v52
	v_or_b32_sdwa v51, v51, v50 dst_sel:DWORD dst_unused:UNUSED_PAD src0_sel:DWORD src1_sel:WORD_1
	v_or_b32_sdwa v50, v52, v56 dst_sel:DWORD dst_unused:UNUSED_PAD src0_sel:DWORD src1_sel:WORD_1
	s_waitcnt lgkmcnt(0)
	v_pk_fma_f32 v[36:37], v[54:55], v[36:37], v[40:41]
	v_pk_fma_f32 v[34:35], v[140:141], v[34:35], v[38:39]
	v_pk_add_f32 v[40:41], v[42:43], 1.0 op_sel_hi:[1,0]
	v_pk_add_f32 v[38:39], v[44:45], 1.0 op_sel_hi:[1,0]
	v_pk_fma_f32 v[40:41], v[34:35], v[40:41], v[60:61]
	v_bfe_u32 v42, v34, 16, 1
	v_cvt_pk_fp8_f32 v145, v40, v41
	v_bfe_u32 v43, v35, 16, 1
	v_bfe_u32 v44, v36, 16, 1
	v_bfe_u32 v45, v37, 16, 1
	v_pk_fma_f32 v[38:39], v[36:37], v[38:39], v[62:63]
	v_add3_u32 v34, v34, v42, s47
	v_add3_u32 v35, v35, v43, s47
	v_add3_u32 v36, v36, v44, s47
	v_add3_u32 v37, v37, v45, s47
	v_and_b32_sdwa v43, v40, v182 dst_sel:DWORD dst_unused:UNUSED_PAD src0_sel:WORD_1 src1_sel:DWORD
	v_and_b32_sdwa v44, v39, v182 dst_sel:DWORD dst_unused:UNUSED_PAD src0_sel:WORD_1 src1_sel:DWORD
	v_and_b32_sdwa v45, v41, v182 dst_sel:DWORD dst_unused:UNUSED_PAD src0_sel:WORD_1 src1_sel:DWORD
	v_cvt_pk_fp8_f32 v145, v38, v39 op_sel:[0,0,1]
	v_and_b32_sdwa v42, v38, v182 dst_sel:DWORD dst_unused:UNUSED_PAD src0_sel:WORD_1 src1_sel:DWORD
	v_lshrrev_b32_e32 v34, 16, v34
	v_lshrrev_b32_e32 v36, 16, v36
	v_add3_u32 v40, v40, v43, s47
	v_add3_u32 v43, v39, v44, s47
	v_add3_u32 v41, v41, v45, s47
	v_add3_u32 v42, v38, v42, s47
	v_and_or_b32 v34, v35, s44, v34
	v_and_or_b32 v35, v37, s44, v36
	v_and_b32_e32 v36, 0xffff0000, v43
	v_and_b32_e32 v37, 0xffff0000, v41
	global_store_dwordx2 v[48:49], v[34:35], off offset:3584
	v_or_b32_sdwa v35, v36, v42 dst_sel:DWORD dst_unused:UNUSED_PAD src0_sel:DWORD src1_sel:WORD_1
	v_or_b32_sdwa v34, v37, v40 dst_sel:DWORD dst_unused:UNUSED_PAD src0_sel:DWORD src1_sel:WORD_1
	ds_write2st64_b64 v146, v[50:51], v[34:35] offset0:6 offset1:7
	global_store_dword v[46:47], v145, off offset:1792
	s_cbranch_vccnz .LBB0_842
.LBB0_840:
	s_or_b32 s7, s50, 1
	s_xor_b64 s[40:41], s[4:5], -1
	s_or_b32 s4, s7, s6
	s_ashr_i32 s5, s4, 31
	s_lshl_b64 s[42:43], s[4:5], 11
	s_lshl_b64 s[52:53], s[4:5], 13
	s_add_u32 s52, s28, s52
	s_addc_u32 s53, s29, s53
	s_lshl_b64 s[4:5], s[4:5], 12
	v_lshl_add_u64 v[34:35], v[74:75], 0, s[4:5]
	v_mov_b32_e32 v184, v149
	global_load_dwordx4 v[128:131], v66, s[8:9]
	global_load_dwordx4 v[132:135], v66, s[8:9] offset:1024
	global_load_dwordx4 v[136:139], v66, s[8:9] offset:2048
	global_load_dwordx4 v[144:147], v66, s[8:9] offset:3072
	global_load_dwordx4 v[166:169], v66, s[56:57]
	global_load_dwordx4 v[170:173], v66, s[56:57] offset:1024
	global_load_dwordx4 v[186:189], v66, s[56:57] offset:2048
	global_load_dwordx4 v[190:193], v66, s[56:57] offset:3072
	global_load_dwordx4 v[50:53], v66, s[52:53] nt
	global_load_dwordx4 v[54:57], v66, s[52:53] offset:1024 nt
	global_load_dwordx2 v[126:127], v[34:35], off nt
	global_load_dwordx2 v[124:125], v[34:35], off offset:512 nt
	global_load_dwordx2 v[120:121], v[34:35], off offset:1024 nt
	global_load_dwordx2 v[118:119], v[34:35], off offset:1536 nt
	global_load_dwordx4 v[62:65], v66, s[52:53] offset:2048 nt
	global_load_dwordx4 v[58:61], v66, s[52:53] offset:3072 nt
	global_load_dwordx4 v[46:49], v76, s[52:53] nt
	global_load_dwordx4 v[42:45], v78, s[52:53] nt
	global_load_dwordx2 v[122:123], v[34:35], off offset:2048 nt
	global_load_dwordx2 v[116:117], v[34:35], off offset:2560 nt
	global_load_dwordx2 v[114:115], v[34:35], off offset:3072 nt
	global_load_dwordx2 v[112:113], v[34:35], off offset:3584 nt
	global_load_dwordx4 v[38:41], v80, s[52:53] nt
	s_nop 0
	global_load_dwordx4 v[34:37], v82, s[52:53] nt
	s_waitcnt vmcnt(16)
	v_lshlrev_b32_e32 v152, 16, v84
	v_lshlrev_b32_e32 v140, 2, v184
	v_ashrrev_i32_e32 v141, 31, v140
	v_lshlrev_b64 v[142:143], 2, v[140:141]
	v_lshl_add_u64 v[150:151], s[8:9], 0, v[142:143]
	v_add_co_u32_e32 v150, vcc, s45, v150
	v_and_b32_e32 v153, 0xffff0000, v84
	s_nop 0
	v_addc_co_u32_e32 v151, vcc, 0, v151, vcc
	v_lshlrev_b32_e32 v154, 16, v85
	v_and_b32_e32 v155, 0xffff0000, v85
	v_lshlrev_b32_e32 v156, 16, v86
	v_and_b32_e32 v157, 0xffff0000, v86
	v_lshlrev_b32_e32 v158, 16, v87
	v_and_b32_e32 v159, 0xffff0000, v87
	v_lshlrev_b32_e32 v160, 16, v88
	v_and_b32_e32 v161, 0xffff0000, v88
	v_lshlrev_b32_e32 v162, 16, v89
	v_and_b32_e32 v163, 0xffff0000, v89
	v_lshlrev_b32_e32 v164, 16, v90
	v_and_b32_e32 v165, 0xffff0000, v90
	v_lshlrev_b32_e32 v194, 16, v91
	v_and_b32_e32 v195, 0xffff0000, v91
	v_lshlrev_b32_e32 v196, 16, v92
	v_and_b32_e32 v197, 0xffff0000, v92
	v_mov_b32_e32 v204, 0
	v_mov_b32_e32 v205, 0
	v_pk_add_f32 v[130:131], v[130:131], 1.0 op_sel_hi:[1,0]
	v_pk_add_f32 v[128:129], v[128:129], 1.0 op_sel_hi:[1,0]
	v_pk_add_f32 v[134:135], v[134:135], 1.0 op_sel_hi:[1,0]
	v_pk_add_f32 v[132:133], v[132:133], 1.0 op_sel_hi:[1,0]
	v_pk_mul_f32 v[128:129], v[128:129], v[152:153]
	v_pk_mul_f32 v[130:131], v[130:131], v[154:155]
	v_pk_add_f32 v[138:139], v[138:139], 1.0 op_sel_hi:[1,0]
	v_pk_add_f32 v[136:137], v[136:137], 1.0 op_sel_hi:[1,0]
	v_pk_mul_f32 v[132:133], v[132:133], v[156:157]
	v_pk_mul_f32 v[134:135], v[134:135], v[158:159]
	v_pk_fma_f32 v[154:155], v[4:5], s[36:37], v[130:131] op_sel_hi:[1,0,1]
	v_pk_fma_f32 v[156:157], v[2:3], s[36:37], v[128:129] op_sel_hi:[1,0,1]
	v_pk_add_f32 v[146:147], v[146:147], 1.0 op_sel_hi:[1,0]
	v_pk_add_f32 v[144:145], v[144:145], 1.0 op_sel_hi:[1,0]
	v_pk_mul_f32 v[136:137], v[136:137], v[160:161]
	v_pk_mul_f32 v[138:139], v[138:139], v[162:163]
	v_pk_fma_f32 v[158:159], v[8:9], s[36:37], v[134:135] op_sel_hi:[1,0,1]
	v_pk_fma_f32 v[160:161], v[6:7], s[36:37], v[132:133] op_sel_hi:[1,0,1]
	v_add_f32_e32 v128, v156, v157
	v_add_f32_e32 v129, v154, v155
	v_pk_mul_f32 v[144:145], v[144:145], v[164:165]
	v_pk_mul_f32 v[146:147], v[146:147], v[194:195]
	v_pk_fma_f32 v[162:163], v[12:13], s[36:37], v[138:139] op_sel_hi:[1,0,1]
	v_pk_fma_f32 v[164:165], v[10:11], s[36:37], v[136:137] op_sel_hi:[1,0,1]
	v_add_f32_e32 v130, v160, v161
	v_add_f32_e32 v131, v158, v159
	v_add_f32_e32 v128, v128, v129
	v_pk_fma_f32 v[150:151], v[16:17], s[36:37], v[146:147] op_sel_hi:[1,0,1]
	v_pk_fma_f32 v[152:153], v[14:15], s[36:37], v[144:145] op_sel_hi:[1,0,1]
	v_add_f32_e32 v132, v164, v165
	v_add_f32_e32 v133, v162, v163
	v_add_f32_e32 v129, v130, v131
	v_add_f32_e32 v128, 0, v128
	v_add_f32_e32 v134, v152, v153
	v_add_f32_e32 v135, v150, v151
	v_add_f32_e32 v130, v132, v133
	v_add_f32_e32 v128, v128, v129
	v_add_f32_e32 v131, v134, v135
	v_add_f32_e32 v128, v128, v130
	v_add_f32_e32 v134, v128, v131
	v_lshlrev_b32_e32 v128, 16, v93
	v_and_b32_e32 v129, 0xffff0000, v93
	v_pk_add_f32 v[130:131], v[168:169], 1.0 op_sel_hi:[1,0]
	v_pk_add_f32 v[132:133], v[166:167], 1.0 op_sel_hi:[1,0]
	v_pk_mul_f32 v[128:129], v[130:131], v[128:129]
	v_pk_mul_f32 v[130:131], v[132:133], v[196:197]
	v_pk_fma_f32 v[144:145], v[20:21], s[36:37], v[128:129] op_sel_hi:[1,0,1]
	v_pk_fma_f32 v[146:147], v[18:19], s[36:37], v[130:131] op_sel_hi:[1,0,1]
	v_add_f32_e32 v129, v144, v145
	v_add_f32_e32 v128, v146, v147
	v_add_f32_e32 v128, v128, v129
	v_add_f32_e32 v148, v134, v128
	v_lshlrev_b32_e32 v128, 16, v94
	v_and_b32_e32 v129, 0xffff0000, v94
	v_lshlrev_b32_e32 v130, 16, v95
	v_and_b32_e32 v131, 0xffff0000, v95
	v_pk_add_f32 v[132:133], v[172:173], 1.0 op_sel_hi:[1,0]
	v_pk_add_f32 v[134:135], v[170:171], 1.0 op_sel_hi:[1,0]
	v_pk_mul_f32 v[130:131], v[132:133], v[130:131]
	v_pk_mul_f32 v[128:129], v[134:135], v[128:129]
	v_pk_fma_f32 v[136:137], v[24:25], s[36:37], v[130:131] op_sel_hi:[1,0,1]
	v_pk_fma_f32 v[138:139], v[22:23], s[36:37], v[128:129] op_sel_hi:[1,0,1]
	v_add_f32_e32 v129, v136, v137
	v_add_f32_e32 v128, v138, v139
	v_add_f32_e32 v128, v128, v129
	v_add_f32_e32 v148, v148, v128
	v_lshlrev_b32_e32 v128, 16, v96
	v_and_b32_e32 v129, 0xffff0000, v96
	v_lshlrev_b32_e32 v130, 16, v97
	v_and_b32_e32 v131, 0xffff0000, v97
	v_pk_add_f32 v[132:133], v[188:189], 1.0 op_sel_hi:[1,0]
	v_pk_add_f32 v[134:135], v[186:187], 1.0 op_sel_hi:[1,0]
	v_pk_mul_f32 v[130:131], v[132:133], v[130:131]
	v_pk_mul_f32 v[132:133], v[134:135], v[128:129]
	v_pk_fma_f32 v[128:129], v[28:29], s[36:37], v[130:131] op_sel_hi:[1,0,1]
	v_pk_fma_f32 v[130:131], v[26:27], s[36:37], v[132:133] op_sel_hi:[1,0,1]
	v_add_f32_e32 v133, v128, v129
	v_add_f32_e32 v132, v130, v131
	v_add_f32_e32 v132, v132, v133
	v_add_f32_e32 v148, v148, v132
	v_lshlrev_b32_e32 v132, 16, v98
	v_and_b32_e32 v133, 0xffff0000, v98
	v_lshlrev_b32_e32 v134, 16, v99
	v_and_b32_e32 v135, 0xffff0000, v99
	v_pk_add_f32 v[166:167], v[192:193], 1.0 op_sel_hi:[1,0]
	v_pk_add_f32 v[168:169], v[190:191], 1.0 op_sel_hi:[1,0]
	v_pk_mul_f32 v[134:135], v[166:167], v[134:135]
	v_pk_mul_f32 v[166:167], v[168:169], v[132:133]
	v_pk_fma_f32 v[132:133], v[32:33], s[36:37], v[134:135] op_sel_hi:[1,0,1]
	v_pk_fma_f32 v[134:135], v[30:31], s[36:37], v[166:167] op_sel_hi:[1,0,1]
	v_add_f32_e32 v167, v132, v133
	v_add_f32_e32 v166, v134, v135
	v_add_f32_e32 v166, v166, v167
	v_add_f32_e32 v148, v148, v166
	v_lshl_add_u64 v[172:173], s[10:11], 0, v[142:143]
	v_lshl_add_u64 v[170:171], s[38:39], 0, v[142:143]
	v_add_f32_dpp v148, v148, v148 quad_perm:[1,0,3,2] row_mask:0xf bank_mask:0xf bound_ctrl:1
	s_nop 1
	v_add_f32_dpp v148, v148, v148 quad_perm:[2,3,0,1] row_mask:0xf bank_mask:0xf bound_ctrl:1
	s_nop 1
	v_add_f32_dpp v148, v148, v148 row_half_mirror row_mask:0xf bank_mask:0xf bound_ctrl:1
	s_nop 1
	v_add_f32_dpp v148, v148, v148 row_mirror row_mask:0xf bank_mask:0xf bound_ctrl:1
	v_mov_b32_e32 v166, v148
	s_nop 1
	v_permlane16_swap_b32_e32 v148, v166
	v_add_f32_e32 v148, v148, v166
	v_mov_b32_e32 v166, v148
	s_nop 1
	v_permlane32_swap_b32_e32 v148, v166
	v_add_f32_e32 v148, v148, v166
	v_fmac_f32_e32 v155, 0xba000000, v148
	v_fmac_f32_e32 v157, 0xba000000, v148
	v_fmamk_f32 v154, v148, 0xba000000, v154
	v_fmamk_f32 v156, v148, 0xba000000, v156
	v_mul_f32_e32 v166, v157, v157
	v_mul_f32_e32 v167, v155, v155
	v_fmac_f32_e32 v166, v156, v156
	v_fmac_f32_e32 v167, v154, v154
	v_fmac_f32_e32 v159, 0xba000000, v148
	v_fmac_f32_e32 v161, 0xba000000, v148
	v_add_f32_e32 v166, v166, v167
	v_fmamk_f32 v158, v148, 0xba000000, v158
	v_fmamk_f32 v160, v148, 0xba000000, v160
	v_mul_f32_e32 v167, v161, v161
	v_mul_f32_e32 v168, v159, v159
	v_fmac_f32_e32 v167, v160, v160
	v_fmac_f32_e32 v168, v158, v158
	v_add_f32_e32 v167, v167, v168
	v_fmac_f32_e32 v163, 0xba000000, v148
	v_fmac_f32_e32 v165, 0xba000000, v148
	v_add_f32_e32 v166, v166, v167
	v_fmamk_f32 v162, v148, 0xba000000, v162
	v_fmamk_f32 v164, v148, 0xba000000, v164
	v_mul_f32_e32 v167, v165, v165
	v_mul_f32_e32 v168, v163, v163
	v_fmac_f32_e32 v167, v164, v164
	v_fmac_f32_e32 v168, v162, v162
	v_add_f32_e32 v167, v167, v168
	v_fmac_f32_e32 v151, 0xba000000, v148
	v_fmac_f32_e32 v153, 0xba000000, v148
	v_add_f32_e32 v166, v167, v166
	v_fmamk_f32 v150, v148, 0xba000000, v150
	v_fmamk_f32 v152, v148, 0xba000000, v152
	v_mul_f32_e32 v167, v153, v153
	v_mul_f32_e32 v168, v151, v151
	v_fmac_f32_e32 v167, v152, v152
	v_fmac_f32_e32 v168, v150, v150
	v_add_f32_e32 v167, v167, v168
	v_fmac_f32_e32 v145, 0xba000000, v148
	v_fmac_f32_e32 v147, 0xba000000, v148
	v_add_f32_e32 v166, v167, v166
	v_fmamk_f32 v144, v148, 0xba000000, v144
	v_fmamk_f32 v146, v148, 0xba000000, v146
	v_mul_f32_e32 v167, v147, v147
	v_mul_f32_e32 v168, v145, v145
	v_fmac_f32_e32 v167, v146, v146
	v_fmac_f32_e32 v168, v144, v144
	v_add_f32_e32 v167, v167, v168
	v_fmac_f32_e32 v137, 0xba000000, v148
	v_fmac_f32_e32 v139, 0xba000000, v148
	v_add_f32_e32 v166, v167, v166
	v_fmamk_f32 v136, v148, 0xba000000, v136
	v_fmamk_f32 v138, v148, 0xba000000, v138
	v_mul_f32_e32 v167, v139, v139
	v_mul_f32_e32 v168, v137, v137
	v_fmac_f32_e32 v167, v138, v138
	v_fmac_f32_e32 v168, v136, v136
	v_add_f32_e32 v167, v167, v168
	v_fmac_f32_e32 v129, 0xba000000, v148
	v_fmac_f32_e32 v131, 0xba000000, v148
	v_add_f32_e32 v166, v167, v166
	v_fmamk_f32 v128, v148, 0xba000000, v128
	v_fmamk_f32 v130, v148, 0xba000000, v130
	v_mul_f32_e32 v167, v131, v131
	v_mul_f32_e32 v168, v129, v129
	v_fmac_f32_e32 v167, v130, v130
	v_fmac_f32_e32 v168, v128, v128
	v_add_f32_e32 v167, v167, v168
	v_fmac_f32_e32 v133, 0xba000000, v148
	v_fmac_f32_e32 v135, 0xba000000, v148
	v_add_f32_e32 v166, v167, v166
	v_fmamk_f32 v132, v148, 0xba000000, v132
	v_fmamk_f32 v134, v148, 0xba000000, v134
	v_mul_f32_e32 v148, v135, v135
	v_mul_f32_e32 v167, v133, v133
	v_fmac_f32_e32 v148, v134, v134
	v_fmac_f32_e32 v167, v132, v132
	v_add_f32_e32 v148, v148, v167
	v_add_f32_e32 v148, v148, v166
	v_lshl_add_u64 v[168:169], s[26:27], 0, v[142:143]
	s_nop 0
	v_add_f32_dpp v148, v148, v148 quad_perm:[1,0,3,2] row_mask:0xf bank_mask:0xf bound_ctrl:1
	s_nop 1
	v_add_f32_dpp v148, v148, v148 quad_perm:[2,3,0,1] row_mask:0xf bank_mask:0xf bound_ctrl:1
	s_nop 1
	v_add_f32_dpp v148, v148, v148 row_half_mirror row_mask:0xf bank_mask:0xf bound_ctrl:1
	s_nop 1
	v_add_f32_dpp v148, v148, v148 row_mirror row_mask:0xf bank_mask:0xf bound_ctrl:1
	v_mov_b32_e32 v166, v148
	s_nop 1
	v_permlane16_swap_b32_e32 v148, v166
	v_add_f32_e32 v148, v148, v166
	v_mov_b32_e32 v185, v148
	v_lshl_add_u64 v[166:167], s[14:15], 0, v[142:143]
	ds_read_b128 v[186:189], v243 offset:0
	ds_read_b128 v[190:193], v243 offset:8192
	ds_read_b128 v[194:197], v243 offset:16384
	v_mov_b32_e32 v198, v208
	v_mov_b32_e32 v199, v209
	v_mov_b32_e32 v200, v210
	v_mov_b32_e32 v201, v211
	v_permlane32_swap_b32_e32 v148, v185
	v_add_f32_e32 v142, v148, v185
	v_fmamk_f32 v142, v142, 0x3a000000, v176
	v_mul_f32_e32 v143, 0x4f800000, v142
	v_cmp_gt_f32_e32 vcc, s46, v142
	s_nop 1
	v_cndmask_b32_e32 v142, v142, v143, vcc
	v_sqrt_f32_e32 v143, v142
	s_nop 0
	v_add_u32_e32 v148, -1, v143
	v_fma_f32 v185, -v148, v143, v142
	v_cmp_ge_f32_e64 s[4:5], 0, v185
	v_add_u32_e32 v185, 1, v143
	s_nop 0
	v_cndmask_b32_e64 v148, v143, v148, s[4:5]
	v_fma_f32 v143, -v185, v143, v142
	v_cmp_lt_f32_e64 s[4:5], 0, v143
	s_nop 1
	v_cndmask_b32_e64 v143, v148, v185, s[4:5]
	v_mul_f32_e32 v148, 0x37800000, v143
	v_cndmask_b32_e32 v143, v143, v148, vcc
	v_cmp_class_f32_e32 vcc, v142, v177
	s_nop 1
	v_cndmask_b32_e32 v142, v143, v142, vcc
	v_div_scale_f32 v143, s[4:5], v142, v142, 1.0
	v_rcp_f32_e32 v148, v143
	s_or_b32 s4, s50, s6
	s_ashr_i32 s5, s4, 31
	s_lshl_b64 s[52:53], s[4:5], 11
	v_fma_f32 v185, -v143, v148, 1.0
	v_fmac_f32_e32 v148, v185, v148
	v_div_scale_f32 v185, vcc, 1.0, v142, 1.0
	v_mul_f32_e32 v202, v185, v148
	v_fma_f32 v203, -v143, v202, v185
	v_fmac_f32_e32 v202, v203, v148
	v_fma_f32 v143, -v143, v202, v185
	v_div_fmas_f32 v143, v143, v148, v202
	v_div_fixup_f32 v148, v143, v142, 1.0
	v_pk_mul_f32 v[142:143], v[156:157], v[148:149] op_sel_hi:[1,0]
	v_pk_mul_f32 v[154:155], v[154:155], v[148:149] op_sel_hi:[1,0]
	s_lshl_b64 s[4:5], s[4:5], 12
	s_add_u32 s4, s21, s4
	s_addc_u32 s5, s22, s5
	s_add_u32 s52, s23, s52
	s_addc_u32 s53, s24, s53
	v_pk_mul_f32 v[160:161], v[160:161], v[148:149] op_sel_hi:[1,0]
	v_pk_mul_f32 v[158:159], v[158:159], v[148:149] op_sel_hi:[1,0]
	v_pk_mul_f32 v[164:165], v[164:165], v[148:149] op_sel_hi:[1,0]
	v_pk_mul_f32 v[162:163], v[162:163], v[148:149] op_sel_hi:[1,0]
	v_pk_mul_f32 v[152:153], v[152:153], v[148:149] op_sel_hi:[1,0]
	v_pk_mul_f32 v[150:151], v[150:151], v[148:149] op_sel_hi:[1,0]
	v_pk_mul_f32 v[146:147], v[146:147], v[148:149] op_sel_hi:[1,0]
	v_pk_mul_f32 v[144:145], v[144:145], v[148:149] op_sel_hi:[1,0]
	v_pk_mul_f32 v[138:139], v[138:139], v[148:149] op_sel_hi:[1,0]
	v_pk_mul_f32 v[136:137], v[136:137], v[148:149] op_sel_hi:[1,0]
	v_pk_mul_f32 v[130:131], v[130:131], v[148:149] op_sel_hi:[1,0]
	v_pk_mul_f32 v[202:203], v[132:133], v[148:149] op_sel_hi:[1,0]
	v_pk_mul_f32 v[128:129], v[128:129], v[148:149] op_sel_hi:[1,0]
	s_waitcnt lgkmcnt(0)
	v_pk_fma_f32 v[142:143], v[186:187], v[142:143], v[190:191]
	v_pk_fma_f32 v[156:157], v[188:189], v[154:155], v[192:193]
	v_bfe_u32 v154, v142, 16, 1
	v_add3_u32 v154, v142, v154, s47
	v_bfe_u32 v155, v143, 16, 1
	v_lshrrev_b32_e32 v154, 16, v154
	v_add3_u32 v155, v143, v155, s47
	v_and_or_b32 v186, v155, s44, v154
	v_bfe_u32 v154, v156, 16, 1
	v_add3_u32 v154, v156, v154, s47
	v_lshrrev_b32_e32 v185, 16, v154
	v_bfe_u32 v154, v157, 16, 1
	v_add3_u32 v187, v157, v154, s47
	v_pk_add_f32 v[154:155], v[194:195], 1.0 op_sel_hi:[1,0]
	v_mov_b32_e32 v188, 0
	v_pk_fma_f32 v[154:155], v[154:155], v[142:143], v[198:199]
	v_pk_add_f32 v[142:143], v[196:197], 1.0 op_sel_hi:[1,0]
	v_cvt_pk_fp8_f32 v188, v154, v155
	v_pk_fma_f32 v[156:157], v[142:143], v[156:157], v[200:201]
	v_and_or_b32 v187, v187, s44, v185
	v_lshl_add_u64 v[142:143], v[140:141], 1, s[4:5]
	v_cvt_pk_fp8_f32 v188, v156, v157 op_sel:[0,0,1]
	v_lshl_add_u64 v[140:141], s[52:53], 0, v[140:141]
	global_store_dwordx2 v[142:143], v[186:187], off
	s_or_b32 s4, s50, s25
	global_store_dword v[140:141], v188, off
	ds_read_b128 v[186:189], v243 offset:1024
	s_nop 0
	ds_read_b128 v[190:193], v243 offset:9216
	ds_read_b128 v[194:197], v243 offset:17408
	v_mov_b32_e32 v198, v212
	v_mov_b32_e32 v199, v213
	v_mov_b32_e32 v200, v214
	v_mov_b32_e32 v201, v215
	s_mulk_i32 s4, 0x1010
	s_add_i32 s4, s4, 0
	v_lshl_add_u32 v206, v184, 3, s4
	v_and_b32_sdwa v132, v156, v182 dst_sel:DWORD dst_unused:UNUSED_PAD src0_sel:WORD_1 src1_sel:DWORD
	v_and_b32_sdwa v133, v154, v182 dst_sel:DWORD dst_unused:UNUSED_PAD src0_sel:WORD_1 src1_sel:DWORD
	s_waitcnt lgkmcnt(0)
	v_pk_fma_f32 v[188:189], v[158:159], v[188:189], v[192:193]
	v_pk_fma_f32 v[158:159], v[160:161], v[186:187], v[190:191]
	v_mov_b32_e32 v190, 0
	v_bfe_u32 v160, v158, 16, 1
	v_add3_u32 v160, v158, v160, s47
	v_bfe_u32 v161, v159, 16, 1
	v_lshrrev_b32_e32 v160, 16, v160
	v_add3_u32 v161, v159, v161, s47
	v_and_or_b32 v186, v161, s44, v160
	v_bfe_u32 v160, v188, 16, 1
	v_add3_u32 v160, v188, v160, s47
	v_lshrrev_b32_e32 v185, 16, v160
	v_pk_add_f32 v[160:161], v[194:195], 1.0 op_sel_hi:[1,0]
	v_bfe_u32 v187, v189, 16, 1
	v_pk_fma_f32 v[158:159], v[158:159], v[160:161], v[198:199]
	v_pk_add_f32 v[160:161], v[196:197], 1.0 op_sel_hi:[1,0]
	v_cvt_pk_fp8_f32 v190, v158, v159
	v_pk_fma_f32 v[160:161], v[188:189], v[160:161], v[200:201]
	v_add3_u32 v187, v189, v187, s47
	v_and_or_b32 v187, v187, s44, v185
	v_cvt_pk_fp8_f32 v190, v160, v161 op_sel:[0,0,1]
	global_store_dwordx2 v[142:143], v[186:187], off offset:512
	global_store_dword v[140:141], v190, off offset:256
	ds_read_b128 v[186:189], v243 offset:2048
	s_nop 0
	ds_read_b128 v[190:193], v243 offset:10240
	ds_read_b128 v[194:197], v243 offset:18432
	v_mov_b32_e32 v198, v216
	v_mov_b32_e32 v199, v217
	v_mov_b32_e32 v200, v218
	v_mov_b32_e32 v201, v219
	v_mov_b32_e32 v185, 0
	s_waitcnt lgkmcnt(0)
	v_pk_fma_f32 v[186:187], v[164:165], v[186:187], v[190:191]
	v_pk_add_f32 v[164:165], v[194:195], 1.0 op_sel_hi:[1,0]
	v_pk_fma_f32 v[188:189], v[162:163], v[188:189], v[192:193]
	v_pk_fma_f32 v[164:165], v[186:187], v[164:165], v[198:199]
	v_pk_add_f32 v[162:163], v[196:197], 1.0 op_sel_hi:[1,0]
	v_cvt_pk_fp8_f32 v185, v164, v165
	v_bfe_u32 v190, v186, 16, 1
	v_bfe_u32 v192, v188, 16, 1
	v_pk_fma_f32 v[162:163], v[188:189], v[162:163], v[200:201]
	v_bfe_u32 v191, v187, 16, 1
	v_bfe_u32 v193, v189, 16, 1
	v_add3_u32 v186, v186, v190, s47
	v_add3_u32 v188, v188, v192, s47
	v_cvt_pk_fp8_f32 v185, v162, v163 op_sel:[0,0,1]
	v_add3_u32 v187, v187, v191, s47
	v_add3_u32 v189, v189, v193, s47
	v_lshrrev_b32_e32 v186, 16, v186
	v_lshrrev_b32_e32 v188, 16, v188
	v_and_or_b32 v186, v187, s44, v186
	v_and_or_b32 v187, v189, s44, v188
	global_store_dwordx2 v[142:143], v[186:187], off offset:1024
	global_store_dword v[140:141], v185, off offset:512
	ds_read_b128 v[186:189], v243 offset:3072
	s_nop 0
	ds_read_b128 v[190:193], v243 offset:11264
	ds_read_b128 v[194:197], v243 offset:19456
	v_mov_b32_e32 v198, v220
	v_mov_b32_e32 v199, v221
	v_mov_b32_e32 v200, v222
	v_mov_b32_e32 v201, v223
	v_mov_b32_e32 v185, 0
	v_add_co_u32_e32 v166, vcc, s45, v166
	s_waitcnt lgkmcnt(0)
	v_pk_fma_f32 v[186:187], v[152:153], v[186:187], v[190:191]
	v_pk_add_f32 v[152:153], v[194:195], 1.0 op_sel_hi:[1,0]
	v_addc_co_u32_e32 v167, vcc, 0, v167, vcc
	v_pk_fma_f32 v[152:153], v[186:187], v[152:153], v[198:199]
	v_pk_fma_f32 v[188:189], v[150:151], v[188:189], v[192:193]
	v_cvt_pk_fp8_f32 v185, v152, v153
	v_pk_add_f32 v[150:151], v[196:197], 1.0 op_sel_hi:[1,0]
	v_add_co_u32_e32 v168, vcc, s45, v168
	v_bfe_u32 v190, v186, 16, 1
	v_bfe_u32 v192, v188, 16, 1
	v_pk_fma_f32 v[150:151], v[188:189], v[150:151], v[200:201]
	v_addc_co_u32_e32 v169, vcc, 0, v169, vcc
	v_bfe_u32 v191, v187, 16, 1
	v_bfe_u32 v193, v189, 16, 1
	v_add3_u32 v186, v186, v190, s47
	v_add3_u32 v188, v188, v192, s47
	v_cvt_pk_fp8_f32 v185, v150, v151 op_sel:[0,0,1]
	v_add3_u32 v187, v187, v191, s47
	v_add3_u32 v189, v189, v193, s47
	v_lshrrev_b32_e32 v186, 16, v186
	v_lshrrev_b32_e32 v188, 16, v188
	v_add_co_u32_e32 v172, vcc, s45, v172
	v_and_or_b32 v186, v187, s44, v186
	v_and_or_b32 v187, v189, s44, v188
	v_addc_co_u32_e32 v173, vcc, 0, v173, vcc
	global_store_dwordx2 v[142:143], v[186:187], off offset:1536
	global_store_dword v[140:141], v185, off offset:768
	v_add_co_u32_e32 v170, vcc, s45, v170
	ds_read_b128 v[186:189], v243 offset:4096
	ds_read_b128 v[190:193], v243 offset:12288
	ds_read_b128 v[194:197], v243 offset:20480
	v_addc_co_u32_e32 v171, vcc, 0, v171, vcc
	v_mov_b32_e32 v198, v224
	v_mov_b32_e32 v199, v225
	v_mov_b32_e32 v200, v226
	v_mov_b32_e32 v201, v227
	v_mov_b32_e32 v185, 0
	s_and_b64 vcc, exec, s[40:41]
	s_waitcnt lgkmcnt(0)
	v_pk_fma_f32 v[186:187], v[146:147], v[186:187], v[190:191]
	v_pk_add_f32 v[146:147], v[194:195], 1.0 op_sel_hi:[1,0]
	v_pk_fma_f32 v[188:189], v[144:145], v[188:189], v[192:193]
	v_pk_add_f32 v[144:145], v[196:197], 1.0 op_sel_hi:[1,0]
	v_pk_fma_f32 v[146:147], v[186:187], v[146:147], v[198:199]
	v_bfe_u32 v190, v186, 16, 1
	v_cvt_pk_fp8_f32 v185, v146, v147
	v_bfe_u32 v192, v188, 16, 1
	v_pk_fma_f32 v[144:145], v[188:189], v[144:145], v[200:201]
	v_bfe_u32 v191, v187, 16, 1
	v_bfe_u32 v193, v189, 16, 1
	v_add3_u32 v186, v186, v190, s47
	v_add3_u32 v188, v188, v192, s47
	v_cvt_pk_fp8_f32 v185, v144, v145 op_sel:[0,0,1]
	v_add3_u32 v187, v187, v191, s47
	v_add3_u32 v189, v189, v193, s47
	v_lshrrev_b32_e32 v186, 16, v186
	v_lshrrev_b32_e32 v188, 16, v188
	v_and_or_b32 v186, v187, s44, v186
	v_and_or_b32 v187, v189, s44, v188
	global_store_dwordx2 v[142:143], v[186:187], off offset:2048
	global_store_dword v[140:141], v185, off offset:1024
	ds_read_b128 v[186:189], v243 offset:5120
	s_nop 0
	ds_read_b128 v[190:193], v243 offset:13312
	ds_read_b128 v[194:197], v243 offset:21504
	v_mov_b32_e32 v198, v228
	v_mov_b32_e32 v199, v229
	v_mov_b32_e32 v200, v230
	v_mov_b32_e32 v201, v231
	v_mov_b32_e32 v185, 0
	s_waitcnt lgkmcnt(0)
	v_pk_fma_f32 v[136:137], v[136:137], v[188:189], v[192:193]
	v_pk_fma_f32 v[138:139], v[138:139], v[186:187], v[190:191]
	v_pk_add_f32 v[188:189], v[194:195], 1.0 op_sel_hi:[1,0]
	v_pk_add_f32 v[186:187], v[196:197], 1.0 op_sel_hi:[1,0]
	v_pk_fma_f32 v[198:199], v[138:139], v[188:189], v[198:199]
	v_bfe_u32 v190, v138, 16, 1
	v_cvt_pk_fp8_f32 v185, v198, v199
	v_bfe_u32 v192, v136, 16, 1
	v_pk_fma_f32 v[200:201], v[136:137], v[186:187], v[200:201]
	v_bfe_u32 v191, v139, 16, 1
	v_bfe_u32 v193, v137, 16, 1
	v_add3_u32 v138, v138, v190, s47
	v_add3_u32 v136, v136, v192, s47
	v_cvt_pk_fp8_f32 v185, v200, v201 op_sel:[0,0,1]
	v_add3_u32 v139, v139, v191, s47
	v_add3_u32 v137, v137, v193, s47
	v_lshrrev_b32_e32 v138, 16, v138
	v_lshrrev_b32_e32 v186, 16, v136
	v_and_or_b32 v136, v139, s44, v138
	v_and_or_b32 v137, v137, s44, v186
	global_store_dwordx2 v[142:143], v[136:137], off offset:2560
	global_store_dword v[140:141], v185, off offset:1280
	ds_read_b128 v[136:139], v243 offset:6144
	s_nop 0
	ds_read_b128 v[186:189], v243 offset:14336
	ds_read_b128 v[190:193], v243 offset:22528
	v_mov_b32_e32 v194, v232
	v_mov_b32_e32 v195, v233
	v_mov_b32_e32 v196, v234
	v_mov_b32_e32 v197, v235
	v_pk_mul_f32 v[184:185], v[134:135], v[148:149] op_sel_hi:[1,0]
	v_and_b32_sdwa v134, v157, v182 dst_sel:DWORD dst_unused:UNUSED_PAD src0_sel:WORD_1 src1_sel:DWORD
	v_and_b32_sdwa v135, v155, v182 dst_sel:DWORD dst_unused:UNUSED_PAD src0_sel:WORD_1 src1_sel:DWORD
	v_add3_u32 v148, v154, v133, s47
	v_add3_u32 v154, v156, v132, s47
	v_add3_u32 v132, v157, v134, s47
	v_add3_u32 v133, v155, v135, s47
	v_and_b32_e32 v155, 0xffff0000, v132
	v_and_b32_e32 v156, 0xffff0000, v133
	s_waitcnt lgkmcnt(0)
	v_pk_fma_f32 v[130:131], v[130:131], v[136:137], v[186:187]
	v_pk_add_f32 v[134:135], v[190:191], 1.0 op_sel_hi:[1,0]
	v_pk_fma_f32 v[128:129], v[128:129], v[138:139], v[188:189]
	v_pk_fma_f32 v[188:189], v[130:131], v[134:135], v[194:195]
	v_pk_add_f32 v[132:133], v[192:193], 1.0 op_sel_hi:[1,0]
	v_cvt_pk_fp8_f32 v204, v188, v189
	v_bfe_u32 v136, v130, 16, 1
	v_bfe_u32 v138, v128, 16, 1
	v_pk_fma_f32 v[186:187], v[128:129], v[132:133], v[196:197]
	v_bfe_u32 v137, v131, 16, 1
	v_bfe_u32 v139, v129, 16, 1
	v_add3_u32 v130, v130, v136, s47
	v_add3_u32 v128, v128, v138, s47
	v_cvt_pk_fp8_f32 v204, v186, v187 op_sel:[0,0,1]
	v_add3_u32 v131, v131, v137, s47
	v_add3_u32 v129, v129, v139, s47
	v_lshrrev_b32_e32 v130, 16, v130
	v_lshrrev_b32_e32 v132, 16, v128
	v_and_or_b32 v128, v131, s44, v130
	v_and_or_b32 v129, v129, s44, v132
	global_store_dwordx2 v[142:143], v[128:129], off offset:3072
	global_store_dword v[140:141], v204, off offset:1536
	ds_read_b128 v[128:131], v243 offset:7168
	s_nop 0
	ds_read_b128 v[132:135], v243 offset:15360
	ds_read_b128 v[136:139], v243 offset:23552
	v_or_b32_sdwa v167, v155, v154 dst_sel:DWORD dst_unused:UNUSED_PAD src0_sel:DWORD src1_sel:WORD_1
	v_or_b32_sdwa v166, v156, v148 dst_sel:DWORD dst_unused:UNUSED_PAD src0_sel:DWORD src1_sel:WORD_1
	v_mov_b32_e32 v154, v236
	v_mov_b32_e32 v155, v237
	v_mov_b32_e32 v156, v238
	v_mov_b32_e32 v157, v239
	v_and_b32_sdwa v148, v160, v182 dst_sel:DWORD dst_unused:UNUSED_PAD src0_sel:WORD_1 src1_sel:DWORD
	v_and_b32_sdwa v169, v161, v182 dst_sel:DWORD dst_unused:UNUSED_PAD src0_sel:WORD_1 src1_sel:DWORD
	v_and_b32_sdwa v172, v159, v182 dst_sel:DWORD dst_unused:UNUSED_PAD src0_sel:WORD_1 src1_sel:DWORD
	v_and_b32_sdwa v168, v158, v182 dst_sel:DWORD dst_unused:UNUSED_PAD src0_sel:WORD_1 src1_sel:DWORD
	v_add3_u32 v148, v160, v148, s47
	v_add3_u32 v160, v161, v169, s47
	v_add3_u32 v159, v159, v172, s47
	v_add3_u32 v158, v158, v168, s47
	v_and_b32_e32 v160, 0xffff0000, v160
	v_and_b32_e32 v161, 0xffff0000, v159
	v_or_b32_sdwa v159, v160, v148 dst_sel:DWORD dst_unused:UNUSED_PAD src0_sel:DWORD src1_sel:WORD_1
	v_or_b32_sdwa v158, v161, v158 dst_sel:DWORD dst_unused:UNUSED_PAD src0_sel:DWORD src1_sel:WORD_1
	ds_write2st64_b64 v206, v[166:167], v[158:159] offset1:1
	v_and_b32_sdwa v159, v163, v182 dst_sel:DWORD dst_unused:UNUSED_PAD src0_sel:WORD_1 src1_sel:DWORD
	v_and_b32_sdwa v148, v162, v182 dst_sel:DWORD dst_unused:UNUSED_PAD src0_sel:WORD_1 src1_sel:DWORD
	v_and_b32_sdwa v160, v165, v182 dst_sel:DWORD dst_unused:UNUSED_PAD src0_sel:WORD_1 src1_sel:DWORD
	v_add3_u32 v159, v163, v159, s47
	v_and_b32_sdwa v158, v164, v182 dst_sel:DWORD dst_unused:UNUSED_PAD src0_sel:WORD_1 src1_sel:DWORD
	v_add3_u32 v148, v162, v148, s47
	v_add3_u32 v160, v165, v160, s47
	v_and_b32_e32 v159, 0xffff0000, v159
	v_add3_u32 v158, v164, v158, s47
	v_and_b32_e32 v160, 0xffff0000, v160
	v_or_b32_sdwa v159, v159, v148 dst_sel:DWORD dst_unused:UNUSED_PAD src0_sel:DWORD src1_sel:WORD_1
	v_and_b32_sdwa v148, v150, v182 dst_sel:DWORD dst_unused:UNUSED_PAD src0_sel:WORD_1 src1_sel:DWORD
	v_and_b32_sdwa v161, v151, v182 dst_sel:DWORD dst_unused:UNUSED_PAD src0_sel:WORD_1 src1_sel:DWORD
	v_and_b32_sdwa v162, v153, v182 dst_sel:DWORD dst_unused:UNUSED_PAD src0_sel:WORD_1 src1_sel:DWORD
	v_or_b32_sdwa v158, v160, v158 dst_sel:DWORD dst_unused:UNUSED_PAD src0_sel:DWORD src1_sel:WORD_1
	v_and_b32_sdwa v160, v152, v182 dst_sel:DWORD dst_unused:UNUSED_PAD src0_sel:WORD_1 src1_sel:DWORD
	v_add3_u32 v148, v150, v148, s47
	v_add3_u32 v150, v151, v161, s47
	v_add3_u32 v151, v153, v162, s47
	v_add3_u32 v152, v152, v160, s47
	v_and_b32_e32 v150, 0xffff0000, v150
	v_and_b32_e32 v153, 0xffff0000, v151
	v_or_b32_sdwa v151, v150, v148 dst_sel:DWORD dst_unused:UNUSED_PAD src0_sel:DWORD src1_sel:WORD_1
	v_or_b32_sdwa v150, v153, v152 dst_sel:DWORD dst_unused:UNUSED_PAD src0_sel:DWORD src1_sel:WORD_1
	ds_write2st64_b64 v206, v[158:159], v[150:151] offset0:2 offset1:3
	v_and_b32_sdwa v151, v145, v182 dst_sel:DWORD dst_unused:UNUSED_PAD src0_sel:WORD_1 src1_sel:DWORD
	v_and_b32_sdwa v152, v147, v182 dst_sel:DWORD dst_unused:UNUSED_PAD src0_sel:WORD_1 src1_sel:DWORD
	v_and_b32_sdwa v148, v144, v182 dst_sel:DWORD dst_unused:UNUSED_PAD src0_sel:WORD_1 src1_sel:DWORD
	v_and_b32_sdwa v150, v146, v182 dst_sel:DWORD dst_unused:UNUSED_PAD src0_sel:WORD_1 src1_sel:DWORD
	v_add3_u32 v145, v145, v151, s47
	v_add3_u32 v147, v147, v152, s47
	v_add3_u32 v146, v146, v150, s47
	v_add3_u32 v144, v144, v148, s47
	v_and_b32_e32 v145, 0xffff0000, v145
	v_and_b32_e32 v147, 0xffff0000, v147
	v_or_b32_sdwa v145, v145, v144 dst_sel:DWORD dst_unused:UNUSED_PAD src0_sel:DWORD src1_sel:WORD_1
	v_or_b32_sdwa v144, v147, v146 dst_sel:DWORD dst_unused:UNUSED_PAD src0_sel:DWORD src1_sel:WORD_1
	v_and_b32_sdwa v147, v198, v182 dst_sel:DWORD dst_unused:UNUSED_PAD src0_sel:WORD_1 src1_sel:DWORD
	v_and_b32_sdwa v148, v201, v182 dst_sel:DWORD dst_unused:UNUSED_PAD src0_sel:WORD_1 src1_sel:DWORD
	v_and_b32_sdwa v150, v199, v182 dst_sel:DWORD dst_unused:UNUSED_PAD src0_sel:WORD_1 src1_sel:DWORD
	v_and_b32_sdwa v146, v200, v182 dst_sel:DWORD dst_unused:UNUSED_PAD src0_sel:WORD_1 src1_sel:DWORD
	v_add3_u32 v151, v198, v147, s47
	v_add3_u32 v147, v201, v148, s47
	v_add3_u32 v148, v199, v150, s47
	v_add3_u32 v146, v200, v146, s47
	v_and_b32_e32 v147, 0xffff0000, v147
	v_and_b32_e32 v148, 0xffff0000, v148
	v_or_b32_sdwa v147, v147, v146 dst_sel:DWORD dst_unused:UNUSED_PAD src0_sel:DWORD src1_sel:WORD_1
	v_or_b32_sdwa v146, v148, v151 dst_sel:DWORD dst_unused:UNUSED_PAD src0_sel:DWORD src1_sel:WORD_1
	ds_write2st64_b64 v206, v[144:145], v[146:147] offset0:4 offset1:5
	v_and_b32_sdwa v145, v188, v182 dst_sel:DWORD dst_unused:UNUSED_PAD src0_sel:WORD_1 src1_sel:DWORD
	v_and_b32_sdwa v146, v187, v182 dst_sel:DWORD dst_unused:UNUSED_PAD src0_sel:WORD_1 src1_sel:DWORD
	v_and_b32_sdwa v147, v189, v182 dst_sel:DWORD dst_unused:UNUSED_PAD src0_sel:WORD_1 src1_sel:DWORD
	v_and_b32_sdwa v144, v186, v182 dst_sel:DWORD dst_unused:UNUSED_PAD src0_sel:WORD_1 src1_sel:DWORD
	v_add3_u32 v148, v188, v145, s47
	v_add3_u32 v145, v187, v146, s47
	v_add3_u32 v146, v189, v147, s47
	v_add3_u32 v144, v186, v144, s47
	v_and_b32_e32 v145, 0xffff0000, v145
	v_and_b32_e32 v146, 0xffff0000, v146
	v_or_b32_sdwa v145, v145, v144 dst_sel:DWORD dst_unused:UNUSED_PAD src0_sel:DWORD src1_sel:WORD_1
	v_or_b32_sdwa v144, v146, v148 dst_sel:DWORD dst_unused:UNUSED_PAD src0_sel:DWORD src1_sel:WORD_1
	s_waitcnt lgkmcnt(0)
	v_pk_fma_f32 v[130:131], v[202:203], v[130:131], v[134:135]
	v_pk_fma_f32 v[128:129], v[184:185], v[128:129], v[132:133]
	v_pk_add_f32 v[134:135], v[136:137], 1.0 op_sel_hi:[1,0]
	v_pk_add_f32 v[132:133], v[138:139], 1.0 op_sel_hi:[1,0]
	v_pk_fma_f32 v[134:135], v[128:129], v[134:135], v[154:155]
	v_bfe_u32 v136, v128, 16, 1
	v_cvt_pk_fp8_f32 v205, v134, v135
	v_bfe_u32 v137, v129, 16, 1
	v_bfe_u32 v138, v130, 16, 1
	v_bfe_u32 v139, v131, 16, 1
	v_pk_fma_f32 v[132:133], v[130:131], v[132:133], v[156:157]
	v_add3_u32 v128, v128, v136, s47
	v_add3_u32 v129, v129, v137, s47
	v_add3_u32 v130, v130, v138, s47
	v_add3_u32 v131, v131, v139, s47
	v_and_b32_sdwa v137, v134, v182 dst_sel:DWORD dst_unused:UNUSED_PAD src0_sel:WORD_1 src1_sel:DWORD
	v_and_b32_sdwa v138, v133, v182 dst_sel:DWORD dst_unused:UNUSED_PAD src0_sel:WORD_1 src1_sel:DWORD
	v_and_b32_sdwa v139, v135, v182 dst_sel:DWORD dst_unused:UNUSED_PAD src0_sel:WORD_1 src1_sel:DWORD
	v_cvt_pk_fp8_f32 v205, v132, v133 op_sel:[0,0,1]
	v_and_b32_sdwa v136, v132, v182 dst_sel:DWORD dst_unused:UNUSED_PAD src0_sel:WORD_1 src1_sel:DWORD
	v_lshrrev_b32_e32 v128, 16, v128
	v_lshrrev_b32_e32 v130, 16, v130
	v_add3_u32 v134, v134, v137, s47
	v_add3_u32 v137, v133, v138, s47
	v_add3_u32 v135, v135, v139, s47
	v_add3_u32 v136, v132, v136, s47
	v_and_or_b32 v128, v129, s44, v128
	v_and_or_b32 v129, v131, s44, v130
	v_and_b32_e32 v130, 0xffff0000, v137
	v_and_b32_e32 v131, 0xffff0000, v135
	global_store_dwordx2 v[142:143], v[128:129], off offset:3584
	v_or_b32_sdwa v129, v130, v136 dst_sel:DWORD dst_unused:UNUSED_PAD src0_sel:DWORD src1_sel:WORD_1
	v_or_b32_sdwa v128, v131, v134 dst_sel:DWORD dst_unused:UNUSED_PAD src0_sel:DWORD src1_sel:WORD_1
	ds_write2st64_b64 v206, v[144:145], v[128:129] offset0:6 offset1:7
	global_store_dword v[140:141], v205, off offset:1792
	global_load_dwordx4 v[132:135], v66, s[8:9]
	global_load_dwordx4 v[136:139], v66, s[8:9] offset:1024
	global_load_dwordx4 v[142:145], v66, s[8:9] offset:2048
	global_load_dwordx4 v[150:153], v66, s[8:9] offset:3072
	global_load_dwordx4 v[154:157], v66, s[56:57]
	global_load_dwordx4 v[158:161], v66, s[56:57] offset:1024
	global_load_dwordx4 v[244:247], v66, s[56:57] offset:2048
	global_load_dwordx4 v[162:165], v66, s[56:57] offset:3072
	s_cbranch_vccnz .Lmy_p7_nold
	global_load_dwordx4 v[2:5], v[102:103], off nt
	global_load_dwordx4 v[6:9], v[102:103], off offset:1024 nt
	global_load_dwordx2 v[84:85], v[100:101], off nt
	global_load_dwordx2 v[86:87], v[100:101], off offset:512 nt
	global_load_dwordx2 v[88:89], v[100:101], off offset:1024 nt
	global_load_dwordx2 v[90:91], v[100:101], off offset:1536 nt
	global_load_dwordx4 v[10:13], v[102:103], off offset:2048 nt
	global_load_dwordx4 v[14:17], v[102:103], off offset:3072 nt
	global_load_dwordx4 v[18:21], v[104:105], off nt
	global_load_dwordx4 v[22:25], v[106:107], off nt
	global_load_dwordx2 v[92:93], v[100:101], off offset:2048 nt
	global_load_dwordx2 v[94:95], v[100:101], off offset:2560 nt
	global_load_dwordx2 v[96:97], v[100:101], off offset:3072 nt
	global_load_dwordx2 v[98:99], v[100:101], off offset:3584 nt
	global_load_dwordx4 v[26:29], v[108:109], off nt
	global_load_dwordx4 v[30:33], v[110:111], off nt
	s_waitcnt vmcnt(16)
	s_branch .LBB0_839
.Lmy_p7_nold:
	s_waitcnt vmcnt(0)
	s_branch .LBB0_839
